# v40 + v_cvt_pk_bf16_f32 instead of the integer RNE pack also in the weight/x conversion code (prologue and tail rounds)
# speedup vs baseline: 1.0157x; 1.0026x over previous
; #define GAS __attribute__((address_space(1)))
; #define LAS __attribute__((address_space(3)))
; __device__ __forceinline__ unsigned pk2(float lo, float hi) { return f2bf(lo) | (f2bf(hi) << 16); }
; template <bool WT> __device__ __forceinline__ void cvt_process(const CvtItem& ci, const CvtLoad& L, LAS float* scr, int lane) {
;     ...
;     for (int j = 0; j < 4; ++j) { const int n = (lane >> 3) + 8 * j; const LAS float* s = scr + (8 * c) * 33 + n;
;         v4u o; o.x = pk2(s[0 * 33] * g0.x, s[1 * 33] * g0.y); o.y = pk2(s[2 * 33] * g0.z, s[3 * 33] * g0.w); o.z = pk2(s[4 * 33] * g1.x, s[5 * 33] * g1.y); o.w = pk2(s[6 * 33] * g1.z, s[7 * 33] * g1.w);
;         GAS v4u* dp = (GAS v4u*)(ci.WT + (size_t)(ci.row_off + wrow_map(ci.mode, n0 + n)) * ci.K + k0 + 8 * c);
;         if constexpr (WT) asm volatile("global_store_dwordx4 %0, %1, off sc1" :: "v"(dp), "v"(o) : "memory"); else if (ci.late) __builtin_nontemporal_store(o, dp); else *dp = o; }
.LBB0_29:
	s_waitcnt lgkmcnt(3)
	v_mov_b32_e32 v20, v13
	s_waitcnt lgkmcnt(2)
	v_mov_b32_e32 v13, v14
	v_mov_b32_e32 v21, v15
	v_pk_mul_f32 v[10:11], v[10:11], v[12:13]
	s_waitcnt lgkmcnt(1)
	v_mov_b32_e32 v12, v3
	s_waitcnt lgkmcnt(0)
	v_mov_b32_e32 v13, v17
	v_pk_mul_f32 v[8:9], v[8:9], v[20:21]
	v_pk_mul_f32 v[4:5], v[4:5], v[12:13]
	v_mov_b32_e32 v3, v16
	v_pk_mul_f32 v[2:3], v[6:7], v[2:3]
	v_cvt_pk_bf16_f32 v4, v2, v4
	v_cvt_pk_bf16_f32 v2, v10, v8
	v_add_u32_e32 v6, s14, v18
	v_cvt_pk_bf16_f32 v5, v3, v5
	v_cvt_pk_bf16_f32 v3, v11, v9
	v_ashrrev_i32_e32 v7, 31, v6
	v_mul_lo_u32 v8, s66, v7
	v_mul_lo_u32 v9, s67, v6
	v_mad_u64_u32 v[6:7], s[4:5], s66, v6, 0
	v_add3_u32 v7, v7, v8, v9
	v_lshl_add_u64 v[6:7], v[6:7], 1, s[68:69]
	v_lshl_add_u64 v[6:7], s[74:75], 1, v[6:7]
	v_lshl_add_u64 v[6:7], v[6:7], 0, v[90:91]
	global_store_dwordx4 v[6:7], v[2:5], off
	s_waitcnt lgkmcnt(0)

; #define GAS __attribute__((address_space(1)))
; #define LAS __attribute__((address_space(3)))
; #define LDS_WAIT() asm volatile("s_waitcnt lgkmcnt(0)" ::: "memory")
; __device__ __forceinline__ unsigned pk2(float lo, float hi) { return f2bf(lo) | (f2bf(hi) << 16); }
; __device__ __forceinline__ int wrow_map(int mode, int n) {
;     ...
;     if (mode == 2) { if (n < DFF) return 256 * (n >> 7) + (n & 127); const int n2 = n - DFF; return 256 * (n2 >> 7) + 128 + (n2 & 127); }
; template <bool WT> __device__ __forceinline__ void cvt_process(const CvtItem& ci, const CvtLoad& L, LAS float* scr, int lane) {
;     ...
;     const int c = lane & 7; const bool hg = ci.gk != nullptr;
;     f32x4 g0, g1;
; #pragma unroll
;     for (int e = 0; e < 4; ++e) { g0[e] = hg ? L.g0[e] : 1.f; g1[e] = hg ? L.g1[e] : 1.f; }
;     LDS_WAIT(); asm volatile("" ::: "memory");
; #pragma unroll
;     for (int j = 0; j < 4; ++j) { const int n = (lane >> 3) + 8 * j; const LAS float* s = scr + (8 * c) * 33 + n;
;         v4u o; o.x = pk2(s[0 * 33] * g0.x, s[1 * 33] * g0.y); o.y = pk2(s[2 * 33] * g0.z, s[3 * 33] * g0.w); o.z = pk2(s[4 * 33] * g1.x, s[5 * 33] * g1.y); o.w = pk2(s[6 * 33] * g1.z, s[7 * 33] * g1.w);
;         GAS v4u* dp = (GAS v4u*)(ci.WT + (size_t)(ci.row_off + wrow_map(ci.mode, n0 + n)) * ci.K + k0 + 8 * c);
;         if constexpr (WT) asm volatile("global_store_dwordx4 %0, %1, off sc1" :: "v"(dp), "v"(o) : "memory"); else if (ci.late) __builtin_nontemporal_store(o, dp); else *dp = o; }
.LBB0_93:
	s_waitcnt vmcnt(4)
	v_cndmask_b32_e64 v97, v88, 1.0, s[92:93]
	v_cndmask_b32_e64 v89, v89, 1.0, s[92:93]
	v_cndmask_b32_e64 v88, v87, 1.0, s[92:93]
	v_cndmask_b32_e64 v87, v84, 1.0, s[92:93]
	v_cndmask_b32_e64 v84, v83, 1.0, s[92:93]
	s_waitcnt lgkmcnt(2)
	v_mov_b32_e32 v83, v104
	v_mov_b32_e32 v104, v99
	v_cndmask_b32_e64 v96, v86, 1.0, s[92:93]
	v_cndmask_b32_e64 v86, v82, 1.0, s[92:93]
	v_cndmask_b32_e64 v85, v85, 1.0, s[92:93]
	v_mov_b32_e32 v82, v98
	v_pk_mul_f32 v[98:99], v[88:89], v[104:105]
	s_waitcnt lgkmcnt(0)
	v_mov_b32_e32 v105, v102
	v_mov_b32_e32 v102, v101
	v_mov_b32_e32 v104, v100
	v_pk_mul_f32 v[100:101], v[84:85], v[102:103]
	v_pk_mul_f32 v[82:83], v[96:97], v[82:83]
	v_pk_mul_f32 v[104:105], v[86:87], v[104:105]
	v_cvt_pk_bf16_f32 v98, v82, v98
	v_add_u32_e32 v82, s36, v90
	v_cvt_pk_bf16_f32 v99, v83, v99
	v_ashrrev_i32_e32 v83, 31, v82
	v_cvt_pk_bf16_f32 v100, v104, v100
	v_mul_lo_u32 v90, s26, v83
	v_mul_lo_u32 v102, s27, v82
	v_mad_u64_u32 v[82:83], s[4:5], s26, v82, 0
	v_add3_u32 v83, v83, v90, v102
	v_lshl_add_u64 v[82:83], v[82:83], 1, s[34:35]
	v_lshl_add_u64 v[82:83], s[84:85], 1, v[82:83]
	v_lshlrev_b32_e32 v90, 1, v92
	v_cvt_pk_bf16_f32 v101, v105, v101
	v_lshl_add_u64 v[82:83], v[82:83], 0, v[90:91]
	global_store_dwordx4 v[82:83], v[98:101], off
	ds_read2_b32 v[82:83], v109 offset0:8 offset1:41
	ds_read2_b32 v[102:103], v109 offset0:74 offset1:107
	ds_read2_b32 v[98:99], v109 offset0:140 offset1:173
	ds_read2_b32 v[100:101], v109 offset0:206 offset1:239
	v_add_u32_e32 v105, s86, v106
	s_cmp_gt_i32 s2, 1
	s_mov_b64 s[88:89], -1
	s_cbranch_scc0 .LBB0_99
	v_cmp_lt_i32_e32 vcc, s37, v105
	v_lshlrev_b32_e32 v126, 1, v105
	v_and_b32_e32 v127, 0x7f, v105
	s_and_saveexec_b64 s[4:5], vcc
	s_xor_b64 s[88:89], exec, s[4:5]
	v_add_u32_e32 v104, 0x7fffea00, v126
	v_and_b32_e32 v104, 0x7fffff00, v104
	v_or3_b32 v104, v127, v104, s0
	s_andn2_saveexec_b64 s[88:89], s[88:89]
	v_and_or_b32 v104, v126, s1, v127
	s_or_b64 exec, exec, s[88:89]
	s_mov_b64 s[88:89], 0

; #define GAS __attribute__((address_space(1)))
; #define LAS __attribute__((address_space(3)))
; __device__ __forceinline__ unsigned pk2(float lo, float hi) { return f2bf(lo) | (f2bf(hi) << 16); }
; __device__ __forceinline__ int wrow_map(int mode, int n) {
;     if (mode == 1) { if (n >= 1024 && n < 2048) { const int d = n & 63; return (n & ~63) + 32 * ((d >> 4) & 1) + 8 * ((d >> 2) & 3) + 4 * (d >> 5) + (d & 3); } return n; }
;     if (mode == 2) { if (n < DFF) return 256 * (n >> 7) + (n & 127); const int n2 = n - DFF; return 256 * (n2 >> 7) + 128 + (n2 & 127); }
;     return n;
; template <bool WT> __device__ __forceinline__ void cvt_process(const CvtItem& ci, const CvtLoad& L, LAS float* scr, int lane) {
;     ...
;     for (int j = 0; j < 4; ++j) { const int n = (lane >> 3) + 8 * j; const LAS float* s = scr + (8 * c) * 33 + n;
;         v4u o; o.x = pk2(s[0 * 33] * g0.x, s[1 * 33] * g0.y); o.y = pk2(s[2 * 33] * g0.z, s[3 * 33] * g0.w); o.z = pk2(s[4 * 33] * g1.x, s[5 * 33] * g1.y); o.w = pk2(s[6 * 33] * g1.z, s[7 * 33] * g1.w);
;         GAS v4u* dp = (GAS v4u*)(ci.WT + (size_t)(ci.row_off + wrow_map(ci.mode, n0 + n)) * ci.K + k0 + 8 * c);
;         if constexpr (WT) asm volatile("global_store_dwordx4 %0, %1, off sc1" :: "v"(dp), "v"(o) : "memory"); else if (ci.late) __builtin_nontemporal_store(o, dp); else *dp = o; }
.LBB0_103:
	s_waitcnt lgkmcnt(2)
	v_mov_b32_e32 v127, v102
	v_mov_b32_e32 v102, v83
	v_mov_b32_e32 v126, v82
	v_pk_mul_f32 v[82:83], v[88:89], v[102:103]
	s_waitcnt lgkmcnt(0)
	v_mov_b32_e32 v103, v100
	v_mov_b32_e32 v100, v99
	v_mov_b32_e32 v102, v98
	v_pk_mul_f32 v[98:99], v[84:85], v[100:101]
	v_pk_mul_f32 v[126:127], v[96:97], v[126:127]
	v_pk_mul_f32 v[102:103], v[86:87], v[102:103]
	v_cvt_pk_bf16_f32 v100, v102, v98
	v_cvt_pk_bf16_f32 v98, v126, v82
	v_add_u32_e32 v82, s36, v104
	v_cvt_pk_bf16_f32 v101, v103, v99
	v_cvt_pk_bf16_f32 v99, v127, v83
	v_ashrrev_i32_e32 v83, 31, v82
	v_mul_lo_u32 v102, s26, v83
	v_mul_lo_u32 v103, s27, v82
	v_mad_u64_u32 v[82:83], s[4:5], s26, v82, 0
	v_add3_u32 v83, v83, v102, v103
	v_lshl_add_u64 v[82:83], v[82:83], 1, s[34:35]
	v_lshl_add_u64 v[82:83], s[84:85], 1, v[82:83]
	v_lshl_add_u64 v[82:83], v[82:83], 0, v[90:91]
	global_store_dwordx4 v[82:83], v[98:101], off
	ds_read2_b32 v[82:83], v109 offset0:16 offset1:49
	ds_read2_b32 v[102:103], v109 offset0:82 offset1:115
	ds_read2_b32 v[98:99], v109 offset0:148 offset1:181
	ds_read2_b32 v[100:101], v109 offset0:214 offset1:247
	v_add_u32_e32 v105, s86, v107
	s_cmp_gt_i32 s2, 1
	s_mov_b64 s[88:89], -1
	s_cbranch_scc0 .LBB0_109
	v_cmp_lt_i32_e32 vcc, s37, v105
	v_lshlrev_b32_e32 v126, 1, v105
	v_and_b32_e32 v127, 0x7f, v105
	s_and_saveexec_b64 s[4:5], vcc
	s_xor_b64 s[88:89], exec, s[4:5]
	v_add_u32_e32 v104, 0x7fffea00, v126
	v_and_b32_e32 v104, 0x7fffff00, v104
	v_or3_b32 v104, v127, v104, s0
	s_andn2_saveexec_b64 s[88:89], s[88:89]
	v_and_or_b32 v104, v126, s1, v127
	s_or_b64 exec, exec, s[88:89]
	s_mov_b64 s[88:89], 0

; #define GAS __attribute__((address_space(1)))
; #define LAS __attribute__((address_space(3)))
; __device__ __forceinline__ unsigned pk2(float lo, float hi) { return f2bf(lo) | (f2bf(hi) << 16); }
; __device__ __forceinline__ int wrow_map(int mode, int n) {
;     if (mode == 1) { if (n >= 1024 && n < 2048) { const int d = n & 63; return (n & ~63) + 32 * ((d >> 4) & 1) + 8 * ((d >> 2) & 3) + 4 * (d >> 5) + (d & 3); } return n; }
;     if (mode == 2) { if (n < DFF) return 256 * (n >> 7) + (n & 127); const int n2 = n - DFF; return 256 * (n2 >> 7) + 128 + (n2 & 127); }
;     return n;
; template <bool WT> __device__ __forceinline__ void cvt_process(const CvtItem& ci, const CvtLoad& L, LAS float* scr, int lane) {
;     ...
;     for (int j = 0; j < 4; ++j) { const int n = (lane >> 3) + 8 * j; const LAS float* s = scr + (8 * c) * 33 + n;
;         v4u o; o.x = pk2(s[0 * 33] * g0.x, s[1 * 33] * g0.y); o.y = pk2(s[2 * 33] * g0.z, s[3 * 33] * g0.w); o.z = pk2(s[4 * 33] * g1.x, s[5 * 33] * g1.y); o.w = pk2(s[6 * 33] * g1.z, s[7 * 33] * g1.w);
;         GAS v4u* dp = (GAS v4u*)(ci.WT + (size_t)(ci.row_off + wrow_map(ci.mode, n0 + n)) * ci.K + k0 + 8 * c);
;         if constexpr (WT) asm volatile("global_store_dwordx4 %0, %1, off sc1" :: "v"(dp), "v"(o) : "memory"); else if (ci.late) __builtin_nontemporal_store(o, dp); else *dp = o; }
.LBB0_113:
	s_waitcnt lgkmcnt(2)
	v_mov_b32_e32 v127, v102
	v_mov_b32_e32 v102, v83
	v_mov_b32_e32 v126, v82
	v_pk_mul_f32 v[82:83], v[88:89], v[102:103]
	s_waitcnt lgkmcnt(0)
	v_mov_b32_e32 v103, v100
	v_mov_b32_e32 v100, v99
	v_mov_b32_e32 v102, v98
	v_pk_mul_f32 v[98:99], v[84:85], v[100:101]
	v_pk_mul_f32 v[126:127], v[96:97], v[126:127]
	v_pk_mul_f32 v[102:103], v[86:87], v[102:103]
	v_cvt_pk_bf16_f32 v100, v102, v98
	v_cvt_pk_bf16_f32 v98, v126, v82
	v_add_u32_e32 v82, s36, v104
	v_cvt_pk_bf16_f32 v101, v103, v99
	v_cvt_pk_bf16_f32 v99, v127, v83
	v_ashrrev_i32_e32 v83, 31, v82
	v_mul_lo_u32 v102, s26, v83
	v_mul_lo_u32 v103, s27, v82
	v_mad_u64_u32 v[82:83], s[4:5], s26, v82, 0
	v_add3_u32 v83, v83, v102, v103
	v_lshl_add_u64 v[82:83], v[82:83], 1, s[34:35]
	v_lshl_add_u64 v[82:83], s[84:85], 1, v[82:83]
	v_lshl_add_u64 v[82:83], v[82:83], 0, v[90:91]
	global_store_dwordx4 v[82:83], v[98:101], off
	ds_read2_b32 v[98:99], v109 offset0:24 offset1:57
	ds_read2_b32 v[100:101], v109 offset0:90 offset1:123
	ds_read2_b32 v[82:83], v109 offset0:156 offset1:189
	ds_read2_b32 v[104:105], v109 offset0:222 offset1:255
	s_cmp_gt_i32 s2, 1
	s_waitcnt lgkmcnt(3)
	v_mov_b32_e32 v102, v99
	s_waitcnt lgkmcnt(2)
	v_mov_b32_e32 v99, v100
	v_mov_b32_e32 v103, v101
	s_waitcnt lgkmcnt(1)
	v_mov_b32_e32 v100, v83
	s_waitcnt lgkmcnt(0)
	v_mov_b32_e32 v83, v104
	v_mov_b32_e32 v101, v105
	v_add_u32_e32 v105, s86, v108
	s_mov_b64 s[86:87], -1
	s_cbranch_scc0 .LBB0_119
	v_cmp_lt_i32_e32 vcc, s37, v105
	v_lshlrev_b32_e32 v126, 1, v105
	v_and_b32_e32 v127, 0x7f, v105
	s_and_saveexec_b64 s[4:5], vcc
	s_xor_b64 s[86:87], exec, s[4:5]
	v_add_u32_e32 v104, 0x7fffea00, v126
	v_and_b32_e32 v104, 0x7fffff00, v104
	v_or3_b32 v104, v127, v104, s0
	s_andn2_saveexec_b64 s[86:87], s[86:87]
	v_and_or_b32 v104, v126, s1, v127
	s_or_b64 exec, exec, s[86:87]
	s_mov_b64 s[86:87], 0

; #define GAS __attribute__((address_space(1)))
; #define LAS __attribute__((address_space(3)))
; #define LDS_WAIT() asm volatile("s_waitcnt lgkmcnt(0)" ::: "memory")
; __device__ __forceinline__ unsigned pk2(float lo, float hi) { return f2bf(lo) | (f2bf(hi) << 16); }
; template <bool WT> __device__ __forceinline__ void cvt_process(const CvtItem& ci, const CvtLoad& L, LAS float* scr, int lane) {
;     ...
;     for (int j = 0; j < 4; ++j) { const int n = (lane >> 3) + 8 * j; const LAS float* s = scr + (8 * c) * 33 + n;
;         v4u o; o.x = pk2(s[0 * 33] * g0.x, s[1 * 33] * g0.y); o.y = pk2(s[2 * 33] * g0.z, s[3 * 33] * g0.w); o.z = pk2(s[4 * 33] * g1.x, s[5 * 33] * g1.y); o.w = pk2(s[6 * 33] * g1.z, s[7 * 33] * g1.w);
;         GAS v4u* dp = (GAS v4u*)(ci.WT + (size_t)(ci.row_off + wrow_map(ci.mode, n0 + n)) * ci.K + k0 + 8 * c);
;         if constexpr (WT) asm volatile("global_store_dwordx4 %0, %1, off sc1" :: "v"(dp), "v"(o) : "memory"); else if (ci.late) __builtin_nontemporal_store(o, dp); else *dp = o; }
;     LDS_WAIT(); asm volatile("" ::: "memory");
.LBB0_123:
	v_pk_mul_f32 v[88:89], v[88:89], v[102:103]
	v_pk_mul_f32 v[84:85], v[84:85], v[100:101]
	v_pk_mul_f32 v[96:97], v[96:97], v[98:99]
	v_pk_mul_f32 v[82:83], v[86:87], v[82:83]
	v_cvt_pk_bf16_f32 v84, v82, v84
	v_cvt_pk_bf16_f32 v82, v96, v88
	v_add_u32_e32 v86, s36, v104
	v_cvt_pk_bf16_f32 v85, v83, v85
	v_cvt_pk_bf16_f32 v83, v97, v89
	v_ashrrev_i32_e32 v87, 31, v86
	v_mul_lo_u32 v88, s26, v87
	v_mul_lo_u32 v89, s27, v86
	v_mad_u64_u32 v[86:87], s[4:5], s26, v86, 0
	v_add3_u32 v87, v87, v88, v89
	v_lshl_add_u64 v[86:87], v[86:87], 1, s[34:35]
	v_lshl_add_u64 v[86:87], s[84:85], 1, v[86:87]
	v_lshl_add_u64 v[86:87], v[86:87], 0, v[90:91]
	global_store_dwordx4 v[86:87], v[82:85], off
	s_waitcnt lgkmcnt(0)
	s_andn2_b64 vcc, exec, s[78:79]
	s_cbranch_vccz .LBB0_125
	s_andn2_b64 vcc, exec, s[20:21]
	s_cbranch_vccnz .LBB0_30
	s_branch .LBB0_166

; #define GAS __attribute__((address_space(1)))
; #define LAS __attribute__((address_space(3)))
; #define LDS_WAIT() asm volatile("s_waitcnt lgkmcnt(0)" ::: "memory")
; __device__ __forceinline__ unsigned pk2(float lo, float hi) { return f2bf(lo) | (f2bf(hi) << 16); }
; __device__ __forceinline__ int wrow_map(int mode, int n) {
;     if (mode == 1) { if (n >= 1024 && n < 2048) { const int d = n & 63; return (n & ~63) + 32 * ((d >> 4) & 1) + 8 * ((d >> 2) & 3) + 4 * (d >> 5) + (d & 3); } return n; }
;     if (mode == 2) { if (n < DFF) return 256 * (n >> 7) + (n & 127); const int n2 = n - DFF; return 256 * (n2 >> 7) + 128 + (n2 & 127); }
;     return n;
; template <bool WT> __device__ __forceinline__ void cvt_process(const CvtItem& ci, const CvtLoad& L, LAS float* scr, int lane) {
;     ...
;     const int c = lane & 7; const bool hg = ci.gk != nullptr;
;     f32x4 g0, g1;
; #pragma unroll
;     for (int e = 0; e < 4; ++e) { g0[e] = hg ? L.g0[e] : 1.f; g1[e] = hg ? L.g1[e] : 1.f; }
;     LDS_WAIT(); asm volatile("" ::: "memory");
; #pragma unroll
;     for (int j = 0; j < 4; ++j) { const int n = (lane >> 3) + 8 * j; const LAS float* s = scr + (8 * c) * 33 + n;
;         v4u o; o.x = pk2(s[0 * 33] * g0.x, s[1 * 33] * g0.y); o.y = pk2(s[2 * 33] * g0.z, s[3 * 33] * g0.w); o.z = pk2(s[4 * 33] * g1.x, s[5 * 33] * g1.y); o.w = pk2(s[6 * 33] * g1.z, s[7 * 33] * g1.w);
;         GAS v4u* dp = (GAS v4u*)(ci.WT + (size_t)(ci.row_off + wrow_map(ci.mode, n0 + n)) * ci.K + k0 + 8 * c);
;         if constexpr (WT) asm volatile("global_store_dwordx4 %0, %1, off sc1" :: "v"(dp), "v"(o) : "memory"); else if (ci.late) __builtin_nontemporal_store(o, dp); else *dp = o; }
.LBB0_135:
	s_waitcnt vmcnt(6)
	v_cndmask_b32_e64 v51, v48, 1.0, s[30:31]
	v_cndmask_b32_e64 v49, v49, 1.0, s[30:31]
	v_cndmask_b32_e64 v48, v47, 1.0, s[30:31]
	v_cndmask_b32_e64 v47, v44, 1.0, s[30:31]
	v_cndmask_b32_e64 v44, v43, 1.0, s[30:31]
	s_waitcnt lgkmcnt(2)
	v_mov_b32_e32 v43, v58
	v_mov_b32_e32 v58, v53
	v_cndmask_b32_e64 v50, v46, 1.0, s[30:31]
	v_cndmask_b32_e64 v46, v42, 1.0, s[30:31]
	v_cndmask_b32_e64 v45, v45, 1.0, s[30:31]
	v_mov_b32_e32 v42, v52
	v_pk_mul_f32 v[52:53], v[48:49], v[58:59]
	s_waitcnt lgkmcnt(0)
	v_mov_b32_e32 v59, v56
	v_mov_b32_e32 v56, v55
	v_mov_b32_e32 v58, v54
	v_pk_mul_f32 v[54:55], v[44:45], v[56:57]
	v_pk_mul_f32 v[42:43], v[50:51], v[42:43]
	v_pk_mul_f32 v[58:59], v[46:47], v[58:59]
	v_cvt_pk_bf16_f32 v52, v42, v52
	v_add_u32_e32 v42, s15, v60
	v_cvt_pk_bf16_f32 v53, v43, v53
	v_ashrrev_i32_e32 v43, 31, v42
	v_cvt_pk_bf16_f32 v55, v59, v55
	v_cvt_pk_bf16_f32 v54, v58, v54
	v_mul_lo_u32 v56, s70, v43
	v_mul_lo_u32 v57, s71, v42
	v_mad_u64_u32 v[42:43], s[4:5], s70, v42, 0
	v_add3_u32 v43, v43, v56, v57
	v_lshl_add_u64 v[42:43], v[42:43], 1, s[72:73]
	v_lshl_add_u64 v[42:43], s[80:81], 1, v[42:43]
	v_lshl_add_u64 v[42:43], v[42:43], 0, v[90:91]
	global_store_dwordx4 v[42:43], v[52:55], off
	ds_read2_b32 v[42:43], v109 offset0:8 offset1:41
	ds_read2_b32 v[56:57], v109 offset0:74 offset1:107
	ds_read2_b32 v[52:53], v109 offset0:140 offset1:173
	ds_read2_b32 v[54:55], v109 offset0:206 offset1:239
	v_add_u32_e32 v59, s82, v106
	s_cmp_gt_i32 s13, 1
	s_mov_b64 s[26:27], -1
	s_cbranch_scc0 .LBB0_141
	v_cmp_lt_i32_e32 vcc, s37, v59
	v_lshlrev_b32_e32 v60, 1, v59
	v_and_b32_e32 v61, 0x7f, v59
	s_and_saveexec_b64 s[4:5], vcc
	s_xor_b64 s[26:27], exec, s[4:5]
	v_add_u32_e32 v58, 0x7fffea00, v60
	v_and_b32_e32 v58, 0x7fffff00, v58
	v_or3_b32 v58, v61, v58, s0
	s_andn2_saveexec_b64 s[26:27], s[26:27]
	v_and_or_b32 v58, v60, s1, v61
	s_or_b64 exec, exec, s[26:27]
	s_mov_b64 s[26:27], 0

; #define GAS __attribute__((address_space(1)))
; #define LAS __attribute__((address_space(3)))
; __device__ __forceinline__ unsigned pk2(float lo, float hi) { return f2bf(lo) | (f2bf(hi) << 16); }
; __device__ __forceinline__ int wrow_map(int mode, int n) {
;     if (mode == 1) { if (n >= 1024 && n < 2048) { const int d = n & 63; return (n & ~63) + 32 * ((d >> 4) & 1) + 8 * ((d >> 2) & 3) + 4 * (d >> 5) + (d & 3); } return n; }
;     if (mode == 2) { if (n < DFF) return 256 * (n >> 7) + (n & 127); const int n2 = n - DFF; return 256 * (n2 >> 7) + 128 + (n2 & 127); }
;     return n;
; template <bool WT> __device__ __forceinline__ void cvt_process(const CvtItem& ci, const CvtLoad& L, LAS float* scr, int lane) {
;     ...
;     for (int j = 0; j < 4; ++j) { const int n = (lane >> 3) + 8 * j; const LAS float* s = scr + (8 * c) * 33 + n;
;         v4u o; o.x = pk2(s[0 * 33] * g0.x, s[1 * 33] * g0.y); o.y = pk2(s[2 * 33] * g0.z, s[3 * 33] * g0.w); o.z = pk2(s[4 * 33] * g1.x, s[5 * 33] * g1.y); o.w = pk2(s[6 * 33] * g1.z, s[7 * 33] * g1.w);
;         GAS v4u* dp = (GAS v4u*)(ci.WT + (size_t)(ci.row_off + wrow_map(ci.mode, n0 + n)) * ci.K + k0 + 8 * c);
;         if constexpr (WT) asm volatile("global_store_dwordx4 %0, %1, off sc1" :: "v"(dp), "v"(o) : "memory"); else if (ci.late) __builtin_nontemporal_store(o, dp); else *dp = o; }
.LBB0_145:
	s_waitcnt lgkmcnt(2)
	v_mov_b32_e32 v61, v56
	v_mov_b32_e32 v56, v43
	v_mov_b32_e32 v60, v42
	v_pk_mul_f32 v[42:43], v[48:49], v[56:57]
	s_waitcnt lgkmcnt(0)
	v_mov_b32_e32 v57, v54
	v_mov_b32_e32 v54, v53
	v_mov_b32_e32 v56, v52
	v_pk_mul_f32 v[52:53], v[44:45], v[54:55]
	v_pk_mul_f32 v[60:61], v[50:51], v[60:61]
	v_pk_mul_f32 v[56:57], v[46:47], v[56:57]
	v_cvt_pk_bf16_f32 v54, v56, v52
	v_cvt_pk_bf16_f32 v52, v60, v42
	v_add_u32_e32 v42, s15, v58
	v_cvt_pk_bf16_f32 v55, v57, v53
	v_cvt_pk_bf16_f32 v53, v61, v43
	v_ashrrev_i32_e32 v43, 31, v42
	v_mul_lo_u32 v56, s70, v43
	v_mul_lo_u32 v57, s71, v42
	v_mad_u64_u32 v[42:43], s[4:5], s70, v42, 0
	v_add3_u32 v43, v43, v56, v57
	v_lshl_add_u64 v[42:43], v[42:43], 1, s[72:73]
	v_lshl_add_u64 v[42:43], s[80:81], 1, v[42:43]
	v_lshl_add_u64 v[42:43], v[42:43], 0, v[90:91]
	global_store_dwordx4 v[42:43], v[52:55], off
	ds_read2_b32 v[42:43], v109 offset0:16 offset1:49
	ds_read2_b32 v[56:57], v109 offset0:82 offset1:115
	ds_read2_b32 v[52:53], v109 offset0:148 offset1:181
	ds_read2_b32 v[54:55], v109 offset0:214 offset1:247
	v_add_u32_e32 v59, s82, v107
	s_cmp_gt_i32 s13, 1
	s_mov_b64 s[26:27], -1
	s_cbranch_scc0 .LBB0_151
	v_cmp_lt_i32_e32 vcc, s37, v59
	v_lshlrev_b32_e32 v60, 1, v59
	v_and_b32_e32 v61, 0x7f, v59
	s_and_saveexec_b64 s[4:5], vcc
	s_xor_b64 s[26:27], exec, s[4:5]
	v_add_u32_e32 v58, 0x7fffea00, v60
	v_and_b32_e32 v58, 0x7fffff00, v58
	v_or3_b32 v58, v61, v58, s0
	s_andn2_saveexec_b64 s[26:27], s[26:27]
	v_and_or_b32 v58, v60, s1, v61
	s_or_b64 exec, exec, s[26:27]
	s_mov_b64 s[26:27], 0

; #define GAS __attribute__((address_space(1)))
; #define LAS __attribute__((address_space(3)))
; __device__ __forceinline__ unsigned pk2(float lo, float hi) { return f2bf(lo) | (f2bf(hi) << 16); }
; __device__ __forceinline__ int wrow_map(int mode, int n) {
;     if (mode == 1) { if (n >= 1024 && n < 2048) { const int d = n & 63; return (n & ~63) + 32 * ((d >> 4) & 1) + 8 * ((d >> 2) & 3) + 4 * (d >> 5) + (d & 3); } return n; }
;     if (mode == 2) { if (n < DFF) return 256 * (n >> 7) + (n & 127); const int n2 = n - DFF; return 256 * (n2 >> 7) + 128 + (n2 & 127); }
;     return n;
; template <bool WT> __device__ __forceinline__ void cvt_process(const CvtItem& ci, const CvtLoad& L, LAS float* scr, int lane) {
;     ...
;     for (int j = 0; j < 4; ++j) { const int n = (lane >> 3) + 8 * j; const LAS float* s = scr + (8 * c) * 33 + n;
;         v4u o; o.x = pk2(s[0 * 33] * g0.x, s[1 * 33] * g0.y); o.y = pk2(s[2 * 33] * g0.z, s[3 * 33] * g0.w); o.z = pk2(s[4 * 33] * g1.x, s[5 * 33] * g1.y); o.w = pk2(s[6 * 33] * g1.z, s[7 * 33] * g1.w);
;         GAS v4u* dp = (GAS v4u*)(ci.WT + (size_t)(ci.row_off + wrow_map(ci.mode, n0 + n)) * ci.K + k0 + 8 * c);
;         if constexpr (WT) asm volatile("global_store_dwordx4 %0, %1, off sc1" :: "v"(dp), "v"(o) : "memory"); else if (ci.late) __builtin_nontemporal_store(o, dp); else *dp = o; }
.LBB0_155:
	s_waitcnt lgkmcnt(2)
	v_mov_b32_e32 v61, v56
	v_mov_b32_e32 v56, v43
	v_mov_b32_e32 v60, v42
	v_pk_mul_f32 v[42:43], v[48:49], v[56:57]
	s_waitcnt lgkmcnt(0)
	v_mov_b32_e32 v57, v54
	v_mov_b32_e32 v54, v53
	v_mov_b32_e32 v56, v52
	v_pk_mul_f32 v[52:53], v[44:45], v[54:55]
	v_pk_mul_f32 v[60:61], v[50:51], v[60:61]
	v_pk_mul_f32 v[56:57], v[46:47], v[56:57]
	v_cvt_pk_bf16_f32 v54, v56, v52
	v_cvt_pk_bf16_f32 v52, v60, v42
	v_add_u32_e32 v42, s15, v58
	v_cvt_pk_bf16_f32 v55, v57, v53
	v_cvt_pk_bf16_f32 v53, v61, v43
	v_ashrrev_i32_e32 v43, 31, v42
	v_mul_lo_u32 v56, s70, v43
	v_mul_lo_u32 v57, s71, v42
	v_mad_u64_u32 v[42:43], s[4:5], s70, v42, 0
	v_add3_u32 v43, v43, v56, v57
	v_lshl_add_u64 v[42:43], v[42:43], 1, s[72:73]
	v_lshl_add_u64 v[42:43], s[80:81], 1, v[42:43]
	v_lshl_add_u64 v[42:43], v[42:43], 0, v[90:91]
	global_store_dwordx4 v[42:43], v[52:55], off
	ds_read2_b32 v[52:53], v109 offset0:24 offset1:57
	ds_read2_b32 v[54:55], v109 offset0:90 offset1:123
	ds_read2_b32 v[42:43], v109 offset0:156 offset1:189
	ds_read2_b32 v[56:57], v109 offset0:222 offset1:255
	v_add_u32_e32 v59, s82, v108
	s_cmp_gt_i32 s13, 1
	s_mov_b64 s[26:27], -1
	s_cbranch_scc0 .LBB0_161
	v_cmp_lt_i32_e32 vcc, s37, v59
	v_lshlrev_b32_e32 v60, 1, v59
	v_and_b32_e32 v61, 0x7f, v59
	s_and_saveexec_b64 s[4:5], vcc
	s_xor_b64 s[26:27], exec, s[4:5]
	v_add_u32_e32 v58, 0x7fffea00, v60
	v_and_b32_e32 v58, 0x7fffff00, v58
	v_or3_b32 v58, v61, v58, s0
	s_andn2_saveexec_b64 s[26:27], s[26:27]
	v_and_or_b32 v58, v60, s1, v61
	s_or_b64 exec, exec, s[26:27]
	s_mov_b64 s[26:27], 0

; #define GAS __attribute__((address_space(1)))
; #define LAS __attribute__((address_space(3)))
; #define LDS_WAIT() asm volatile("s_waitcnt lgkmcnt(0)" ::: "memory")
; __device__ __forceinline__ unsigned pk2(float lo, float hi) { return f2bf(lo) | (f2bf(hi) << 16); }
; template <bool WT> __device__ __forceinline__ void cvt_process(const CvtItem& ci, const CvtLoad& L, LAS float* scr, int lane) {
;     ...
;     for (int j = 0; j < 4; ++j) { const int n = (lane >> 3) + 8 * j; const LAS float* s = scr + (8 * c) * 33 + n;
;         v4u o; o.x = pk2(s[0 * 33] * g0.x, s[1 * 33] * g0.y); o.y = pk2(s[2 * 33] * g0.z, s[3 * 33] * g0.w); o.z = pk2(s[4 * 33] * g1.x, s[5 * 33] * g1.y); o.w = pk2(s[6 * 33] * g1.z, s[7 * 33] * g1.w);
;         GAS v4u* dp = (GAS v4u*)(ci.WT + (size_t)(ci.row_off + wrow_map(ci.mode, n0 + n)) * ci.K + k0 + 8 * c);
;         if constexpr (WT) asm volatile("global_store_dwordx4 %0, %1, off sc1" :: "v"(dp), "v"(o) : "memory"); else if (ci.late) __builtin_nontemporal_store(o, dp); else *dp = o; }
;     LDS_WAIT(); asm volatile("" ::: "memory");
.LBB0_165:
	s_waitcnt lgkmcnt(3)
	v_mov_b32_e32 v60, v53
	s_waitcnt lgkmcnt(2)
	v_mov_b32_e32 v53, v54
	v_mov_b32_e32 v61, v55
	v_pk_mul_f32 v[50:51], v[50:51], v[52:53]
	s_waitcnt lgkmcnt(1)
	v_mov_b32_e32 v52, v43
	s_waitcnt lgkmcnt(0)
	v_mov_b32_e32 v53, v57
	v_pk_mul_f32 v[48:49], v[48:49], v[60:61]
	v_pk_mul_f32 v[44:45], v[44:45], v[52:53]
	v_mov_b32_e32 v43, v56
	v_pk_mul_f32 v[42:43], v[46:47], v[42:43]
	v_cvt_pk_bf16_f32 v44, v42, v44
	v_cvt_pk_bf16_f32 v42, v50, v48
	v_add_u32_e32 v46, s15, v58
	v_cvt_pk_bf16_f32 v45, v43, v45
	v_cvt_pk_bf16_f32 v43, v51, v49
	v_ashrrev_i32_e32 v47, 31, v46
	v_mul_lo_u32 v48, s70, v47
	v_mul_lo_u32 v49, s71, v46
	v_mad_u64_u32 v[46:47], s[4:5], s70, v46, 0
	v_add3_u32 v47, v47, v48, v49
	v_lshl_add_u64 v[46:47], v[46:47], 1, s[72:73]
	v_lshl_add_u64 v[46:47], s[80:81], 1, v[46:47]
	v_lshl_add_u64 v[46:47], v[46:47], 0, v[90:91]
	global_store_dwordx4 v[46:47], v[42:45], off
	s_waitcnt lgkmcnt(0)
	s_andn2_b64 vcc, exec, s[20:21]
	s_cbranch_vccnz .LBB0_30

; #define GAS __attribute__((address_space(1)))
; #define LAS __attribute__((address_space(3)))
; #define LDS_WAIT() asm volatile("s_waitcnt lgkmcnt(0)" ::: "memory")
; __device__ __forceinline__ unsigned pk2(float lo, float hi) { return f2bf(lo) | (f2bf(hi) << 16); }
; __device__ __forceinline__ int wrow_map(int mode, int n) {
;     if (mode == 1) { if (n >= 1024 && n < 2048) { const int d = n & 63; return (n & ~63) + 32 * ((d >> 4) & 1) + 8 * ((d >> 2) & 3) + 4 * (d >> 5) + (d & 3); } return n; }
;     if (mode == 2) { if (n < DFF) return 256 * (n >> 7) + (n & 127); const int n2 = n - DFF; return 256 * (n2 >> 7) + 128 + (n2 & 127); }
;     return n;
; template <bool WT> __device__ __forceinline__ void cvt_process(const CvtItem& ci, const CvtLoad& L, LAS float* scr, int lane) {
;     ...
;     const int c = lane & 7; const bool hg = ci.gk != nullptr;
;     f32x4 g0, g1;
; #pragma unroll
;     for (int e = 0; e < 4; ++e) { g0[e] = hg ? L.g0[e] : 1.f; g1[e] = hg ? L.g1[e] : 1.f; }
;     LDS_WAIT(); asm volatile("" ::: "memory");
; #pragma unroll
;     for (int j = 0; j < 4; ++j) { const int n = (lane >> 3) + 8 * j; const LAS float* s = scr + (8 * c) * 33 + n;
;         v4u o; o.x = pk2(s[0 * 33] * g0.x, s[1 * 33] * g0.y); o.y = pk2(s[2 * 33] * g0.z, s[3 * 33] * g0.w); o.z = pk2(s[4 * 33] * g1.x, s[5 * 33] * g1.y); o.w = pk2(s[6 * 33] * g1.z, s[7 * 33] * g1.w);
;         GAS v4u* dp = (GAS v4u*)(ci.WT + (size_t)(ci.row_off + wrow_map(ci.mode, n0 + n)) * ci.K + k0 + 8 * c);
;         if constexpr (WT) asm volatile("global_store_dwordx4 %0, %1, off sc1" :: "v"(dp), "v"(o) : "memory"); else if (ci.late) __builtin_nontemporal_store(o, dp); else *dp = o; }
.LBB0_176:
	s_waitcnt vmcnt(4)
	v_cndmask_b32_e64 v11, v8, 1.0, s[28:29]
	v_cndmask_b32_e64 v9, v9, 1.0, s[28:29]
	v_cndmask_b32_e64 v8, v7, 1.0, s[28:29]
	v_cndmask_b32_e64 v7, v4, 1.0, s[28:29]
	v_cndmask_b32_e64 v4, v3, 1.0, s[28:29]
	s_waitcnt lgkmcnt(2)
	v_mov_b32_e32 v3, v18
	v_mov_b32_e32 v18, v13
	v_cndmask_b32_e64 v10, v6, 1.0, s[28:29]
	v_cndmask_b32_e64 v6, v2, 1.0, s[28:29]
	v_cndmask_b32_e64 v5, v5, 1.0, s[28:29]
	v_mov_b32_e32 v2, v12
	v_pk_mul_f32 v[12:13], v[8:9], v[18:19]
	s_waitcnt lgkmcnt(0)
	v_mov_b32_e32 v19, v16
	v_mov_b32_e32 v16, v15
	v_mov_b32_e32 v18, v14
	v_pk_mul_f32 v[14:15], v[4:5], v[16:17]
	v_pk_mul_f32 v[2:3], v[10:11], v[2:3]
	v_pk_mul_f32 v[18:19], v[6:7], v[18:19]
	v_cvt_pk_bf16_f32 v12, v2, v12
	v_add_u32_e32 v2, s14, v20
	v_cvt_pk_bf16_f32 v13, v3, v13
	v_ashrrev_i32_e32 v3, 31, v2
	v_cvt_pk_bf16_f32 v15, v19, v15
	v_cvt_pk_bf16_f32 v14, v18, v14
	v_mul_lo_u32 v16, s66, v3
	v_mul_lo_u32 v17, s67, v2
	v_mad_u64_u32 v[2:3], s[4:5], s66, v2, 0
	v_add3_u32 v3, v3, v16, v17
	v_lshl_add_u64 v[2:3], v[2:3], 1, s[68:69]
	v_lshl_add_u64 v[2:3], s[74:75], 1, v[2:3]
	v_lshl_add_u64 v[2:3], v[2:3], 0, v[90:91]
	global_store_dwordx4 v[2:3], v[12:15], off
	ds_read2_b32 v[2:3], v109 offset0:8 offset1:41
	ds_read2_b32 v[16:17], v109 offset0:74 offset1:107
	ds_read2_b32 v[12:13], v109 offset0:140 offset1:173
	ds_read2_b32 v[14:15], v109 offset0:206 offset1:239
	v_add_u32_e32 v19, s76, v106
	s_cmp_gt_i32 s12, 1
	s_mov_b64 s[20:21], -1
	s_cbranch_scc0 .LBB0_182
	v_cmp_lt_i32_e32 vcc, s37, v19
	v_lshlrev_b32_e32 v20, 1, v19
	v_and_b32_e32 v21, 0x7f, v19
	s_and_saveexec_b64 s[4:5], vcc
	s_xor_b64 s[20:21], exec, s[4:5]
	v_add_u32_e32 v18, 0x7fffea00, v20
	v_and_b32_e32 v18, 0x7fffff00, v18
	v_or3_b32 v18, v21, v18, s0
	s_andn2_saveexec_b64 s[20:21], s[20:21]
	v_and_or_b32 v18, v20, s1, v21
	s_or_b64 exec, exec, s[20:21]
	s_mov_b64 s[20:21], 0

; #define GAS __attribute__((address_space(1)))
; #define LAS __attribute__((address_space(3)))
; __device__ __forceinline__ unsigned pk2(float lo, float hi) { return f2bf(lo) | (f2bf(hi) << 16); }
; __device__ __forceinline__ int wrow_map(int mode, int n) {
;     if (mode == 1) { if (n >= 1024 && n < 2048) { const int d = n & 63; return (n & ~63) + 32 * ((d >> 4) & 1) + 8 * ((d >> 2) & 3) + 4 * (d >> 5) + (d & 3); } return n; }
;     if (mode == 2) { if (n < DFF) return 256 * (n >> 7) + (n & 127); const int n2 = n - DFF; return 256 * (n2 >> 7) + 128 + (n2 & 127); }
;     return n;
; template <bool WT> __device__ __forceinline__ void cvt_process(const CvtItem& ci, const CvtLoad& L, LAS float* scr, int lane) {
;     ...
;     for (int j = 0; j < 4; ++j) { const int n = (lane >> 3) + 8 * j; const LAS float* s = scr + (8 * c) * 33 + n;
;         v4u o; o.x = pk2(s[0 * 33] * g0.x, s[1 * 33] * g0.y); o.y = pk2(s[2 * 33] * g0.z, s[3 * 33] * g0.w); o.z = pk2(s[4 * 33] * g1.x, s[5 * 33] * g1.y); o.w = pk2(s[6 * 33] * g1.z, s[7 * 33] * g1.w);
;         GAS v4u* dp = (GAS v4u*)(ci.WT + (size_t)(ci.row_off + wrow_map(ci.mode, n0 + n)) * ci.K + k0 + 8 * c);
;         if constexpr (WT) asm volatile("global_store_dwordx4 %0, %1, off sc1" :: "v"(dp), "v"(o) : "memory"); else if (ci.late) __builtin_nontemporal_store(o, dp); else *dp = o; }
.LBB0_186:
	s_waitcnt lgkmcnt(2)
	v_mov_b32_e32 v21, v16
	v_mov_b32_e32 v16, v3
	v_mov_b32_e32 v20, v2
	v_pk_mul_f32 v[2:3], v[8:9], v[16:17]
	s_waitcnt lgkmcnt(0)
	v_mov_b32_e32 v17, v14
	v_mov_b32_e32 v14, v13
	v_mov_b32_e32 v16, v12
	v_pk_mul_f32 v[12:13], v[4:5], v[14:15]
	v_pk_mul_f32 v[20:21], v[10:11], v[20:21]
	v_pk_mul_f32 v[16:17], v[6:7], v[16:17]
	v_cvt_pk_bf16_f32 v14, v16, v12
	v_cvt_pk_bf16_f32 v12, v20, v2
	v_add_u32_e32 v2, s14, v18
	v_cvt_pk_bf16_f32 v15, v17, v13
	v_cvt_pk_bf16_f32 v13, v21, v3
	v_ashrrev_i32_e32 v3, 31, v2
	v_mul_lo_u32 v16, s66, v3
	v_mul_lo_u32 v17, s67, v2
	v_mad_u64_u32 v[2:3], s[4:5], s66, v2, 0
	v_add3_u32 v3, v3, v16, v17
	v_lshl_add_u64 v[2:3], v[2:3], 1, s[68:69]
	v_lshl_add_u64 v[2:3], s[74:75], 1, v[2:3]
	v_lshl_add_u64 v[2:3], v[2:3], 0, v[90:91]
	global_store_dwordx4 v[2:3], v[12:15], off
	ds_read2_b32 v[2:3], v109 offset0:16 offset1:49
	ds_read2_b32 v[16:17], v109 offset0:82 offset1:115
	ds_read2_b32 v[12:13], v109 offset0:148 offset1:181
	ds_read2_b32 v[14:15], v109 offset0:214 offset1:247
	v_add_u32_e32 v19, s76, v107
	s_cmp_gt_i32 s12, 1
	s_mov_b64 s[20:21], -1
	s_cbranch_scc0 .LBB0_192
	v_cmp_lt_i32_e32 vcc, s37, v19
	v_lshlrev_b32_e32 v20, 1, v19
	v_and_b32_e32 v21, 0x7f, v19
	s_and_saveexec_b64 s[4:5], vcc
	s_xor_b64 s[20:21], exec, s[4:5]
	v_add_u32_e32 v18, 0x7fffea00, v20
	v_and_b32_e32 v18, 0x7fffff00, v18
	v_or3_b32 v18, v21, v18, s0
	s_andn2_saveexec_b64 s[20:21], s[20:21]
	v_and_or_b32 v18, v20, s1, v21
	s_or_b64 exec, exec, s[20:21]
	s_mov_b64 s[20:21], 0

; #define GAS __attribute__((address_space(1)))
; #define LAS __attribute__((address_space(3)))
; __device__ __forceinline__ unsigned pk2(float lo, float hi) { return f2bf(lo) | (f2bf(hi) << 16); }
; __device__ __forceinline__ int wrow_map(int mode, int n) {
;     if (mode == 1) { if (n >= 1024 && n < 2048) { const int d = n & 63; return (n & ~63) + 32 * ((d >> 4) & 1) + 8 * ((d >> 2) & 3) + 4 * (d >> 5) + (d & 3); } return n; }
;     if (mode == 2) { if (n < DFF) return 256 * (n >> 7) + (n & 127); const int n2 = n - DFF; return 256 * (n2 >> 7) + 128 + (n2 & 127); }
;     return n;
; template <bool WT> __device__ __forceinline__ void cvt_process(const CvtItem& ci, const CvtLoad& L, LAS float* scr, int lane) {
;     ...
;     for (int j = 0; j < 4; ++j) { const int n = (lane >> 3) + 8 * j; const LAS float* s = scr + (8 * c) * 33 + n;
;         v4u o; o.x = pk2(s[0 * 33] * g0.x, s[1 * 33] * g0.y); o.y = pk2(s[2 * 33] * g0.z, s[3 * 33] * g0.w); o.z = pk2(s[4 * 33] * g1.x, s[5 * 33] * g1.y); o.w = pk2(s[6 * 33] * g1.z, s[7 * 33] * g1.w);
;         GAS v4u* dp = (GAS v4u*)(ci.WT + (size_t)(ci.row_off + wrow_map(ci.mode, n0 + n)) * ci.K + k0 + 8 * c);
;         if constexpr (WT) asm volatile("global_store_dwordx4 %0, %1, off sc1" :: "v"(dp), "v"(o) : "memory"); else if (ci.late) __builtin_nontemporal_store(o, dp); else *dp = o; }
.LBB0_196:
	s_waitcnt lgkmcnt(2)
	v_mov_b32_e32 v21, v16
	v_mov_b32_e32 v16, v3
	v_mov_b32_e32 v20, v2
	v_pk_mul_f32 v[2:3], v[8:9], v[16:17]
	s_waitcnt lgkmcnt(0)
	v_mov_b32_e32 v17, v14
	v_mov_b32_e32 v14, v13
	v_mov_b32_e32 v16, v12
	v_pk_mul_f32 v[12:13], v[4:5], v[14:15]
	v_pk_mul_f32 v[20:21], v[10:11], v[20:21]
	v_pk_mul_f32 v[16:17], v[6:7], v[16:17]
	v_cvt_pk_bf16_f32 v14, v16, v12
	v_cvt_pk_bf16_f32 v12, v20, v2
	v_add_u32_e32 v2, s14, v18
	v_cvt_pk_bf16_f32 v15, v17, v13
	v_cvt_pk_bf16_f32 v13, v21, v3
	v_ashrrev_i32_e32 v3, 31, v2
	v_mul_lo_u32 v16, s66, v3
	v_mul_lo_u32 v17, s67, v2
	v_mad_u64_u32 v[2:3], s[4:5], s66, v2, 0
	v_add3_u32 v3, v3, v16, v17
	v_lshl_add_u64 v[2:3], v[2:3], 1, s[68:69]
	v_lshl_add_u64 v[2:3], s[74:75], 1, v[2:3]
	v_lshl_add_u64 v[2:3], v[2:3], 0, v[90:91]
	global_store_dwordx4 v[2:3], v[12:15], off
	ds_read2_b32 v[12:13], v109 offset0:24 offset1:57
	ds_read2_b32 v[14:15], v109 offset0:90 offset1:123
	ds_read2_b32 v[2:3], v109 offset0:156 offset1:189
	ds_read2_b32 v[16:17], v109 offset0:222 offset1:255
	v_add_u32_e32 v19, s76, v108
	s_cmp_gt_i32 s12, 1
	s_mov_b64 s[20:21], -1
	s_cbranch_scc0 .LBB0_202
	v_cmp_lt_i32_e32 vcc, s37, v19
	v_lshlrev_b32_e32 v20, 1, v19
	v_and_b32_e32 v21, 0x7f, v19
	s_and_saveexec_b64 s[4:5], vcc
	s_xor_b64 s[20:21], exec, s[4:5]
	v_add_u32_e32 v18, 0x7fffea00, v20
	v_and_b32_e32 v18, 0x7fffff00, v18
	v_or3_b32 v18, v21, v18, s0
	s_andn2_saveexec_b64 s[20:21], s[20:21]
	v_and_or_b32 v18, v20, s1, v21
	s_or_b64 exec, exec, s[20:21]
	s_mov_b64 s[20:21], 0

; #define GAS __attribute__((address_space(1)))
; __device__ __forceinline__ unsigned f2bf(float f) { unsigned u = __builtin_bit_cast(unsigned, f); return (u + 0x7fffu + ((u >> 16) & 1u)) >> 16; }
; __device__ __forceinline__ unsigned pk2(float lo, float hi) { return f2bf(lo) | (f2bf(hi) << 16); }
; __device__ __forceinline__ void rows4_to_bf16(int lane, const float* x, bf16* xr_out, float* rsp, int m0, int step) {
;     f32x4 v[4][4];
; #pragma unroll
;     for (int r = 0; r < 4; ++r) { const GAS f32x4* xp = (const GAS f32x4*)(x + (size_t)(m0 + r * step) * DM) + lane;
; #pragma unroll
;         for (int j = 0; j < 4; ++j) v[r][j] = __builtin_nontemporal_load(xp + 64 * j); }
; #pragma unroll
;     for (int r = 0; r < 4; ++r) { float s = 0.f;
; #pragma unroll
;         for (int j = 0; j < 4; ++j) s += (v[r][j].x * v[r][j].x + v[r][j].y * v[r][j].y) + (v[r][j].z * v[r][j].z + v[r][j].w * v[r][j].w);
;         s = wave_sum(s);
;         GAS unsigned long long* o8 = (GAS unsigned long long*)(xr_out + (size_t)(m0 + r * step) * DM) + lane;
; #pragma unroll
;         for (int j = 0; j < 4; ++j) o8[64 * j] = (unsigned long long)pk2(v[r][j].x, v[r][j].y) | ((unsigned long long)pk2(v[r][j].z, v[r][j].w) << 32);
;         if (lane == 0) *(GAS f32x4*)(rsp + (size_t)(m0 + r * step) * 4) = (f32x4){s, 0.f, 0.f, 0.f}; }
; }
.LBB0_292:
	v_lshl_add_u64 v[4:5], s[10:11], 0, v[54:55]
	global_load_dwordx4 v[64:67], v[4:5], off nt
	global_load_dwordx4 v[68:71], v[4:5], off offset:1024 nt
	global_load_dwordx4 v[72:75], v[4:5], off offset:2048 nt
	global_load_dwordx4 v[76:79], v[4:5], off offset:3072 nt
	v_lshl_add_u64 v[4:5], s[14:15], 0, v[54:55]
	v_lshl_add_u64 v[6:7], s[20:21], 0, v[62:63]
	s_add_i32 s26, s23, s16
	s_add_i32 s18, s22, s16
	global_load_dwordx4 v[50:53], v[4:5], off nt
	global_load_dwordx4 v[46:49], v[4:5], off offset:1024 nt
	global_load_dwordx4 v[42:45], v[4:5], off offset:2048 nt
	global_load_dwordx4 v[38:41], v[4:5], off offset:3072 nt
	v_add_co_u32_e64 v4, s[0:1], s30, v6
	s_ashr_i32 s27, s26, 31
	s_ashr_i32 s19, s18, 31
	v_addc_co_u32_e64 v5, s[0:1], 0, v7, s[0:1]
	s_lshl_b64 s[0:1], s[26:27], 12
	s_lshl_b64 s[34:35], s[18:19], 12
	v_lshl_add_u64 v[6:7], v[56:57], 0, s[0:1]
	v_lshl_add_u64 v[8:9], v[56:57], 0, s[34:35]
	global_load_dwordx4 v[34:37], v[6:7], off nt
	global_load_dwordx4 v[30:33], v[6:7], off offset:1024 nt
	global_load_dwordx4 v[26:29], v[6:7], off offset:2048 nt
	global_load_dwordx4 v[22:25], v[6:7], off offset:3072 nt
	global_load_dwordx4 v[18:21], v[8:9], off nt
	global_load_dwordx4 v[14:17], v[8:9], off offset:1024 nt
	global_load_dwordx4 v[10:13], v[8:9], off offset:2048 nt
	s_nop 0
	global_load_dwordx4 v[6:9], v[8:9], off offset:3072 nt
	s_waitcnt vmcnt(15)
	v_mul_f32_e32 v1, v65, v65
	v_mul_f32_e32 v2, v67, v67
	s_waitcnt vmcnt(14)
	v_mul_f32_e32 v80, v69, v69
	v_mul_f32_e32 v81, v71, v71
	s_waitcnt vmcnt(13)
	v_mul_f32_e32 v82, v73, v73
	v_mul_f32_e32 v83, v75, v75
	v_fmac_f32_e32 v1, v64, v64
	v_fmac_f32_e32 v2, v66, v66
	v_fmac_f32_e32 v80, v68, v68
	v_fmac_f32_e32 v81, v70, v70
	s_waitcnt vmcnt(12)
	v_mul_f32_e32 v84, v77, v77
	v_mul_f32_e32 v85, v79, v79
	v_fmac_f32_e32 v82, v72, v72
	v_fmac_f32_e32 v83, v74, v74
	v_add_f32_e32 v1, v1, v2
	v_add_f32_e32 v2, v80, v81
	v_fmac_f32_e32 v84, v76, v76
	v_fmac_f32_e32 v85, v78, v78
	v_add_f32_e32 v80, v82, v83
	v_add_f32_e32 v1, v1, v2
	v_add_f32_e32 v81, v84, v85
	v_add_f32_e32 v1, v1, v80
	v_add_f32_e32 v1, v1, v81
	ds_swizzle_b32 v2, v1 offset:swizzle(SWAP,1)
	v_bfe_u32 v86, v64, 16, 1
	v_bfe_u32 v88, v66, 16, 1
	v_bfe_u32 v92, v70, 16, 1
	v_bfe_u32 v99, v76, 16, 1
	s_waitcnt lgkmcnt(0)
	v_add_f32_e32 v1, v1, v2
	ds_swizzle_b32 v2, v1 offset:swizzle(SWAP,2)
	v_bfe_u32 v101, v78, 16, 1
	v_bfe_u32 v87, v65, 16, 1
	v_bfe_u32 v89, v67, 16, 1
	s_waitcnt lgkmcnt(0)
	v_add_f32_e32 v1, v1, v2
	ds_swizzle_b32 v2, v1 offset:swizzle(SWAP,4)
	v_bfe_u32 v94, v71, 16, 1
	v_bfe_u32 v100, v77, 16, 1
	s_waitcnt lgkmcnt(0)
	v_add_f32_e32 v1, v1, v2
	ds_swizzle_b32 v2, v1 offset:swizzle(SWAP,8)
	v_bfe_u32 v102, v79, 16, 1
	v_add3_u32 v64, v64, v86, s17
	v_add3_u32 v66, v66, v88, s17
	v_add3_u32 v70, v70, v92, s17
	s_waitcnt lgkmcnt(0)
	v_add_f32_e32 v1, v1, v2
	ds_swizzle_b32 v2, v1 offset:swizzle(SWAP,16)
	v_add3_u32 v76, v76, v99, s17
	v_add3_u32 v78, v78, v101, s17
	s_waitcnt lgkmcnt(0)
	v_add_f32_e32 v1, v1, v2
	v_add3_u32 v65, v65, v87, s17
	v_add3_u32 v67, v67, v89, s17
	v_add3_u32 v71, v71, v94, s17
	v_add3_u32 v77, v77, v100, s17
	v_add3_u32 v79, v79, v102, s17
	v_lshrrev_b32_e32 v64, 16, v64
	v_lshrrev_b32_e32 v66, 16, v66
	v_lshrrev_b32_e32 v70, 16, v70
	v_lshrrev_b32_e32 v76, 16, v76
	v_lshrrev_b32_e32 v78, 16, v78
	v_mov_b32_e32 v2, v1
	v_and_or_b32 v64, v65, s29, v64
	v_and_or_b32 v65, v67, s29, v66
	v_and_or_b32 v67, v71, s29, v70
	v_and_or_b32 v70, v77, s29, v76
	v_and_or_b32 v71, v79, s29, v78
	v_permlane32_swap_b32_e32 v1, v2
	v_cvt_pk_bf16_f32 v66, v68, v69
	v_cvt_pk_bf16_f32 v68, v72, v73
	v_cvt_pk_bf16_f32 v69, v74, v75
	global_store_dwordx2 v[4:5], v[64:65], off
	global_store_dwordx2 v[4:5], v[66:67], off offset:512
	global_store_dwordx2 v[4:5], v[68:69], off offset:1024
	global_store_dwordx2 v[4:5], v[70:71], off offset:1536
	s_and_saveexec_b64 s[0:1], vcc
	s_cbranch_execz .LBB0_294
	s_add_u32 s34, s20, s5
	s_addc_u32 s35, s21, s28
	v_add_f32_e32 v2, v1, v2
	v_mov_b32_e32 v4, v3
	v_mov_b32_e32 v5, v3
	global_store_dwordx4 v3, v[2:5], s[34:35]
.LBB0_294:
	s_or_b64 exec, exec, s[0:1]
	s_waitcnt vmcnt(15)
	v_mul_f32_e32 v1, v51, v51
	v_mul_f32_e32 v2, v53, v53
	v_fmac_f32_e32 v1, v50, v50
	v_fmac_f32_e32 v2, v52, v52
	v_add_f32_e32 v1, v1, v2
	s_waitcnt vmcnt(14)
	v_mul_f32_e32 v2, v47, v47
	v_mul_f32_e32 v4, v49, v49
	v_fmac_f32_e32 v2, v46, v46
	v_fmac_f32_e32 v4, v48, v48
	v_add_f32_e32 v2, v2, v4
	v_add_f32_e32 v1, v1, v2
	s_waitcnt vmcnt(13)
	v_mul_f32_e32 v2, v43, v43
	v_mul_f32_e32 v4, v45, v45
	v_fmac_f32_e32 v2, v42, v42
	v_fmac_f32_e32 v4, v44, v44
	v_add_f32_e32 v2, v2, v4
	v_add_f32_e32 v1, v1, v2
	s_waitcnt vmcnt(12)
	v_mul_f32_e32 v2, v39, v39
	v_mul_f32_e32 v4, v41, v41
	v_fmac_f32_e32 v2, v38, v38
	v_fmac_f32_e32 v4, v40, v40
	v_add_f32_e32 v2, v2, v4
	v_add_f32_e32 v1, v1, v2
	ds_swizzle_b32 v2, v1 offset:swizzle(SWAP,1)
	s_waitcnt lgkmcnt(0)
	v_add_f32_e32 v1, v1, v2
	ds_swizzle_b32 v2, v1 offset:swizzle(SWAP,2)
	v_cvt_pk_bf16_f32 v50, v50, v51
	v_lshl_add_u64 v[4:5], s[20:21], 0, v[60:61]
	v_add_co_u32_e64 v4, s[0:1], s30, v4
	v_cvt_pk_bf16_f32 v51, v52, v53
	s_nop 0
	v_addc_co_u32_e64 v5, s[0:1], 0, v5, s[0:1]
	s_waitcnt lgkmcnt(0)
	v_add_f32_e32 v1, v1, v2
	global_store_dwordx2 v[4:5], v[50:51], off
	ds_swizzle_b32 v2, v1 offset:swizzle(SWAP,4)
	v_cvt_pk_bf16_f32 v46, v46, v47
	s_waitcnt lgkmcnt(0)
	v_add_f32_e32 v1, v1, v2
	v_cvt_pk_bf16_f32 v47, v48, v49
	ds_swizzle_b32 v2, v1 offset:swizzle(SWAP,8)
	global_store_dwordx2 v[4:5], v[46:47], off offset:512
	v_cvt_pk_bf16_f32 v42, v42, v43
	s_waitcnt lgkmcnt(0)
	v_add_f32_e32 v1, v1, v2
	ds_swizzle_b32 v2, v1 offset:swizzle(SWAP,16)
	v_cvt_pk_bf16_f32 v43, v44, v45
	global_store_dwordx2 v[4:5], v[42:43], off offset:1024
	v_cvt_pk_bf16_f32 v38, v38, v39
	s_waitcnt lgkmcnt(0)
	v_add_f32_e32 v1, v1, v2
	v_mov_b32_e32 v2, v1
	v_permlane32_swap_b32_e32 v1, v2
	v_cvt_pk_bf16_f32 v39, v40, v41
	global_store_dwordx2 v[4:5], v[38:39], off offset:1536
	s_and_saveexec_b64 s[0:1], vcc
	s_cbranch_execz .LBB0_296
	s_add_u32 s34, s20, s24
	s_addc_u32 s35, s21, s25
	v_add_f32_e32 v2, v1, v2
	v_mov_b32_e32 v4, v3
	v_mov_b32_e32 v5, v3
	global_store_dwordx4 v3, v[2:5], s[34:35]
; #define GAS __attribute__((address_space(1)))
; __device__ __forceinline__ unsigned f2bf(float f) { unsigned u = __builtin_bit_cast(unsigned, f); return (u + 0x7fffu + ((u >> 16) & 1u)) >> 16; }
; __device__ __forceinline__ unsigned pk2(float lo, float hi) { return f2bf(lo) | (f2bf(hi) << 16); }
; __device__ __forceinline__ void rows4_to_bf16(int lane, const float* x, bf16* xr_out, float* rsp, int m0, int step) {
;     f32x4 v[4][4];
; #pragma unroll
;     for (int r = 0; r < 4; ++r) { const GAS f32x4* xp = (const GAS f32x4*)(x + (size_t)(m0 + r * step) * DM) + lane;
; #pragma unroll
;         for (int j = 0; j < 4; ++j) v[r][j] = __builtin_nontemporal_load(xp + 64 * j); }
; #pragma unroll
;     for (int r = 0; r < 4; ++r) { float s = 0.f;
; #pragma unroll
;         for (int j = 0; j < 4; ++j) s += (v[r][j].x * v[r][j].x + v[r][j].y * v[r][j].y) + (v[r][j].z * v[r][j].z + v[r][j].w * v[r][j].w);
;         s = wave_sum(s);
;         GAS unsigned long long* o8 = (GAS unsigned long long*)(xr_out + (size_t)(m0 + r * step) * DM) + lane;
; #pragma unroll
;         for (int j = 0; j < 4; ++j) o8[64 * j] = (unsigned long long)pk2(v[r][j].x, v[r][j].y) | ((unsigned long long)pk2(v[r][j].z, v[r][j].w) << 32);
;         if (lane == 0) *(GAS f32x4*)(rsp + (size_t)(m0 + r * step) * 4) = (f32x4){s, 0.f, 0.f, 0.f}; }
; }
.LBB0_296:
	s_or_b64 exec, exec, s[0:1]
	s_waitcnt vmcnt(15)
	v_mul_f32_e32 v1, v35, v35
	v_mul_f32_e32 v2, v37, v37
	v_fmac_f32_e32 v1, v34, v34
	v_fmac_f32_e32 v2, v36, v36
	v_add_f32_e32 v1, v1, v2
	s_waitcnt vmcnt(14)
	v_mul_f32_e32 v2, v31, v31
	v_mul_f32_e32 v4, v33, v33
	v_fmac_f32_e32 v2, v30, v30
	v_fmac_f32_e32 v4, v32, v32
	v_add_f32_e32 v2, v2, v4
	v_add_f32_e32 v1, v1, v2
	s_waitcnt vmcnt(13)
	v_mul_f32_e32 v2, v27, v27
	v_mul_f32_e32 v4, v29, v29
	v_fmac_f32_e32 v2, v26, v26
	v_fmac_f32_e32 v4, v28, v28
	v_add_f32_e32 v2, v2, v4
	v_add_f32_e32 v1, v1, v2
	s_waitcnt vmcnt(12)
	v_mul_f32_e32 v2, v23, v23
	v_mul_f32_e32 v4, v25, v25
	v_fmac_f32_e32 v2, v22, v22
	v_fmac_f32_e32 v4, v24, v24
	v_add_f32_e32 v2, v2, v4
	v_add_f32_e32 v1, v1, v2
	ds_swizzle_b32 v2, v1 offset:swizzle(SWAP,1)
	s_waitcnt lgkmcnt(0)
	v_add_f32_e32 v1, v1, v2
	ds_swizzle_b32 v2, v1 offset:swizzle(SWAP,2)
	v_cvt_pk_bf16_f32 v34, v34, v35
	s_lshl_b64 s[0:1], s[26:27], 11
	v_lshl_add_u64 v[4:5], v[58:59], 0, s[0:1]
	v_cvt_pk_bf16_f32 v35, v36, v37
	s_waitcnt lgkmcnt(0)
	v_add_f32_e32 v1, v1, v2
	global_store_dwordx2 v[4:5], v[34:35], off
	ds_swizzle_b32 v2, v1 offset:swizzle(SWAP,4)
	v_cvt_pk_bf16_f32 v30, v30, v31
	s_waitcnt lgkmcnt(0)
	v_add_f32_e32 v1, v1, v2
	v_cvt_pk_bf16_f32 v31, v32, v33
	ds_swizzle_b32 v2, v1 offset:swizzle(SWAP,8)
	global_store_dwordx2 v[4:5], v[30:31], off offset:512
	v_cvt_pk_bf16_f32 v26, v26, v27
	s_waitcnt lgkmcnt(0)
	v_add_f32_e32 v1, v1, v2
	ds_swizzle_b32 v2, v1 offset:swizzle(SWAP,16)
	v_cvt_pk_bf16_f32 v27, v28, v29
	global_store_dwordx2 v[4:5], v[26:27], off offset:1024
	v_cvt_pk_bf16_f32 v22, v22, v23
	s_waitcnt lgkmcnt(0)
	v_add_f32_e32 v1, v1, v2
	v_mov_b32_e32 v2, v1
	v_permlane32_swap_b32_e32 v1, v2
	v_cvt_pk_bf16_f32 v23, v24, v25
	global_store_dwordx2 v[4:5], v[22:23], off offset:1536
	s_and_saveexec_b64 s[0:1], vcc
	s_cbranch_execz .LBB0_298
	s_lshl_b64 s[26:27], s[26:27], 4
	s_add_u32 s26, s2, s26
	s_addc_u32 s27, s3, s27
	v_add_f32_e32 v2, v1, v2
	v_mov_b32_e32 v4, v3
	v_mov_b32_e32 v5, v3
	global_store_dwordx4 v3, v[2:5], s[26:27]
.LBB0_298:
	s_or_b64 exec, exec, s[0:1]
	s_waitcnt vmcnt(15)
	v_mul_f32_e32 v1, v19, v19
	v_mul_f32_e32 v2, v21, v21
	v_fmac_f32_e32 v1, v18, v18
	v_fmac_f32_e32 v2, v20, v20
	v_add_f32_e32 v1, v1, v2
	s_waitcnt vmcnt(14)
	v_mul_f32_e32 v2, v15, v15
	v_mul_f32_e32 v4, v17, v17
	v_fmac_f32_e32 v2, v14, v14
	v_fmac_f32_e32 v4, v16, v16
	v_add_f32_e32 v2, v2, v4
	v_add_f32_e32 v1, v1, v2
	s_waitcnt vmcnt(13)
	v_mul_f32_e32 v2, v11, v11
	v_mul_f32_e32 v4, v13, v13
	v_fmac_f32_e32 v2, v10, v10
	v_fmac_f32_e32 v4, v12, v12
	v_add_f32_e32 v2, v2, v4
	v_add_f32_e32 v1, v1, v2
	s_waitcnt vmcnt(12)
	v_mul_f32_e32 v2, v7, v7
	v_mul_f32_e32 v4, v9, v9
	v_fmac_f32_e32 v2, v6, v6
	v_fmac_f32_e32 v4, v8, v8
	v_add_f32_e32 v2, v2, v4
	v_add_f32_e32 v1, v1, v2
	ds_swizzle_b32 v2, v1 offset:swizzle(SWAP,1)
	s_waitcnt lgkmcnt(0)
	v_add_f32_e32 v1, v1, v2
	ds_swizzle_b32 v2, v1 offset:swizzle(SWAP,2)
	v_cvt_pk_bf16_f32 v18, v18, v19
	s_lshl_b64 s[0:1], s[18:19], 11
	v_lshl_add_u64 v[4:5], v[58:59], 0, s[0:1]
	v_cvt_pk_bf16_f32 v19, v20, v21
	s_waitcnt lgkmcnt(0)
	v_add_f32_e32 v1, v1, v2
	global_store_dwordx2 v[4:5], v[18:19], off
	ds_swizzle_b32 v2, v1 offset:swizzle(SWAP,4)
	v_cvt_pk_bf16_f32 v14, v14, v15
	s_waitcnt lgkmcnt(0)
	v_add_f32_e32 v1, v1, v2
	v_cvt_pk_bf16_f32 v15, v16, v17
	ds_swizzle_b32 v2, v1 offset:swizzle(SWAP,8)
	global_store_dwordx2 v[4:5], v[14:15], off offset:512
	v_cvt_pk_bf16_f32 v10, v10, v11
	s_waitcnt lgkmcnt(0)
	v_add_f32_e32 v1, v1, v2
	ds_swizzle_b32 v2, v1 offset:swizzle(SWAP,16)
	v_cvt_pk_bf16_f32 v11, v12, v13
	global_store_dwordx2 v[4:5], v[10:11], off offset:1024
	v_cvt_pk_bf16_f32 v6, v6, v7
	s_waitcnt lgkmcnt(0)
	v_add_f32_e32 v1, v1, v2
	v_mov_b32_e32 v2, v1
	v_permlane32_swap_b32_e32 v1, v2
	v_cvt_pk_bf16_f32 v7, v8, v9
	global_store_dwordx2 v[4:5], v[6:7], off offset:1536
	s_and_saveexec_b64 s[0:1], vcc
	s_cbranch_execz .LBB0_291
	s_lshl_b64 s[18:19], s[18:19], 4
	s_add_u32 s18, s2, s18
	s_addc_u32 s19, s3, s19
	v_add_f32_e32 v2, v1, v2
	v_mov_b32_e32 v4, v3
	v_mov_b32_e32 v5, v3
	global_store_dwordx4 v3, v[2:5], s[18:19]
	s_branch .LBB0_291

; #define GAS __attribute__((address_space(1)))
; #define LAS __attribute__((address_space(3)))
; #define LDS_WAIT() asm volatile("s_waitcnt lgkmcnt(0)" ::: "memory")
; __device__ __forceinline__ unsigned pk2(float lo, float hi) { return f2bf(lo) | (f2bf(hi) << 16); }
; template <bool WT> __device__ __forceinline__ void cvt_process(const CvtItem& ci, const CvtLoad& L, LAS float* scr, int lane) {
;     ...
;     for (int j = 0; j < 4; ++j) { const int n = (lane >> 3) + 8 * j; const LAS float* s = scr + (8 * c) * 33 + n;
;         v4u o; o.x = pk2(s[0 * 33] * g0.x, s[1 * 33] * g0.y); o.y = pk2(s[2 * 33] * g0.z, s[3 * 33] * g0.w); o.z = pk2(s[4 * 33] * g1.x, s[5 * 33] * g1.y); o.w = pk2(s[6 * 33] * g1.z, s[7 * 33] * g1.w);
;         GAS v4u* dp = (GAS v4u*)(ci.WT + (size_t)(ci.row_off + wrow_map(ci.mode, n0 + n)) * ci.K + k0 + 8 * c);
;         if constexpr (WT) asm volatile("global_store_dwordx4 %0, %1, off sc1" :: "v"(dp), "v"(o) : "memory"); else if (ci.late) __builtin_nontemporal_store(o, dp); else *dp = o; }
;     LDS_WAIT(); asm volatile("" ::: "memory");
.LBB0_552:
	s_waitcnt lgkmcnt(3)
	v_mov_b32_e32 v22, v15
	s_waitcnt lgkmcnt(2)
	v_mov_b32_e32 v15, v16
	v_mov_b32_e32 v23, v17
	v_pk_mul_f32 v[12:13], v[12:13], v[14:15]
	s_waitcnt lgkmcnt(1)
	v_mov_b32_e32 v14, v5
	s_waitcnt lgkmcnt(0)
	v_mov_b32_e32 v15, v19
	v_pk_mul_f32 v[10:11], v[10:11], v[22:23]
	v_pk_mul_f32 v[6:7], v[6:7], v[14:15]
	v_mov_b32_e32 v5, v18
	v_pk_mul_f32 v[4:5], v[8:9], v[4:5]
	v_cvt_pk_bf16_f32 v6, v4, v6
	v_cvt_pk_bf16_f32 v4, v12, v10
	v_add_u32_e32 v8, s23, v20
	v_cvt_pk_bf16_f32 v7, v5, v7
	v_cvt_pk_bf16_f32 v5, v13, v11
	v_ashrrev_i32_e32 v9, 31, v8
	v_mul_lo_u32 v10, s86, v9
	v_mul_lo_u32 v11, s87, v8
	v_mad_u64_u32 v[8:9], s[0:1], s86, v8, 0
	v_add3_u32 v9, v9, v10, v11
	v_lshl_add_u64 v[8:9], v[8:9], 1, s[88:89]
	v_lshl_add_u64 v[8:9], s[34:35], 1, v[8:9]
	v_lshl_add_u64 v[8:9], v[8:9], 0, v[2:3]
	global_store_dwordx4 v[8:9], v[4:7], off sc1
	s_waitcnt lgkmcnt(0)

; #define GAS __attribute__((address_space(1)))
; #define LAS __attribute__((address_space(3)))
; #define LDS_WAIT() asm volatile("s_waitcnt lgkmcnt(0)" ::: "memory")
; __device__ __forceinline__ unsigned pk2(float lo, float hi) { return f2bf(lo) | (f2bf(hi) << 16); }
; __device__ __forceinline__ int wrow_map(int mode, int n) {
;     if (mode == 1) { if (n >= 1024 && n < 2048) { const int d = n & 63; return (n & ~63) + 32 * ((d >> 4) & 1) + 8 * ((d >> 2) & 3) + 4 * (d >> 5) + (d & 3); } return n; }
;     if (mode == 2) { if (n < DFF) return 256 * (n >> 7) + (n & 127); const int n2 = n - DFF; return 256 * (n2 >> 7) + 128 + (n2 & 127); }
;     return n;
; template <bool WT> __device__ __forceinline__ void cvt_process(const CvtItem& ci, const CvtLoad& L, LAS float* scr, int lane) {
;     ...
;     const int c = lane & 7; const bool hg = ci.gk != nullptr;
;     f32x4 g0, g1;
; #pragma unroll
;     for (int e = 0; e < 4; ++e) { g0[e] = hg ? L.g0[e] : 1.f; g1[e] = hg ? L.g1[e] : 1.f; }
;     LDS_WAIT(); asm volatile("" ::: "memory");
; #pragma unroll
;     for (int j = 0; j < 4; ++j) { const int n = (lane >> 3) + 8 * j; const LAS float* s = scr + (8 * c) * 33 + n;
;         v4u o; o.x = pk2(s[0 * 33] * g0.x, s[1 * 33] * g0.y); o.y = pk2(s[2 * 33] * g0.z, s[3 * 33] * g0.w); o.z = pk2(s[4 * 33] * g1.x, s[5 * 33] * g1.y); o.w = pk2(s[6 * 33] * g1.z, s[7 * 33] * g1.w);
;         GAS v4u* dp = (GAS v4u*)(ci.WT + (size_t)(ci.row_off + wrow_map(ci.mode, n0 + n)) * ci.K + k0 + 8 * c);
;         if constexpr (WT) asm volatile("global_store_dwordx4 %0, %1, off sc1" :: "v"(dp), "v"(o) : "memory"); else if (ci.late) __builtin_nontemporal_store(o, dp); else *dp = o; }
.LBB0_618:
	v_cndmask_b32_e64 v93, v90, 1.0, s[8:9]
	v_cndmask_b32_e64 v91, v91, 1.0, s[8:9]
	v_cndmask_b32_e64 v90, v89, 1.0, s[8:9]
	v_cndmask_b32_e64 v89, v86, 1.0, s[8:9]
	v_cndmask_b32_e64 v86, v85, 1.0, s[8:9]
	s_waitcnt lgkmcnt(2)
	v_mov_b32_e32 v85, v100
	v_mov_b32_e32 v100, v95
	v_cndmask_b32_e64 v92, v88, 1.0, s[8:9]
	v_cndmask_b32_e64 v88, v84, 1.0, s[8:9]
	v_cndmask_b32_e64 v87, v87, 1.0, s[8:9]
	v_mov_b32_e32 v84, v94
	v_pk_mul_f32 v[94:95], v[90:91], v[100:101]
	s_waitcnt lgkmcnt(0)
	v_mov_b32_e32 v101, v98
	v_mov_b32_e32 v98, v97
	v_mov_b32_e32 v100, v96
	v_pk_mul_f32 v[96:97], v[86:87], v[98:99]
	v_pk_mul_f32 v[84:85], v[92:93], v[84:85]
	v_pk_mul_f32 v[100:101], v[88:89], v[100:101]
	v_add_u32_e32 v2, s19, v2
	v_cvt_pk_bf16_f32 v94, v84, v94
	v_ashrrev_i32_e32 v84, 31, v2
	v_cvt_pk_bf16_f32 v97, v101, v97
	v_cvt_pk_bf16_f32 v96, v100, v96
	v_cvt_pk_bf16_f32 v95, v85, v95
	v_mul_lo_u32 v98, s94, v84
	v_mul_lo_u32 v99, s95, v2
	v_mad_u64_u32 v[84:85], s[8:9], s94, v2, 0
	v_add3_u32 v85, v85, v98, v99
	v_lshl_add_u64 v[84:85], v[84:85], 1, s[96:97]
	v_lshl_add_u64 v[84:85], s[30:31], 1, v[84:85]
	v_lshlrev_b32_e32 v2, 1, v124
	v_lshl_add_u64 v[84:85], v[84:85], 0, v[2:3]
	global_store_dwordx4 v[84:85], v[94:97], off sc1
	ds_read2_b32 v[84:85], v135 offset0:8 offset1:41
	ds_read2_b32 v[98:99], v135 offset0:74 offset1:107
	ds_read2_b32 v[94:95], v135 offset0:140 offset1:173
	ds_read2_b32 v[96:97], v135 offset0:206 offset1:239
	v_add_u32_e32 v100, s0, v132
	s_cmp_gt_i32 s18, 1
	s_mov_b64 s[8:9], -1
	s_cbranch_scc0 .LBB0_624
	s_movk_i32 s1, 0xaff
	v_cmp_lt_i32_e32 vcc, s1, v100
	v_lshlrev_b32_e32 v114, 1, v100
	v_and_b32_e32 v113, 0x7f, v100
	s_and_saveexec_b64 s[8:9], vcc
	s_xor_b64 s[8:9], exec, s[8:9]
	v_add_u32_e32 v101, 0x7fffea00, v114
	v_and_b32_e32 v101, 0x7fffff00, v101
	s_movk_i32 s1, 0x80
	v_or3_b32 v101, v113, v101, s1
	s_andn2_saveexec_b64 s[8:9], s[8:9]
	s_movk_i32 s1, 0xff00
	v_and_or_b32 v101, v114, s1, v113
	s_or_b64 exec, exec, s[8:9]
	s_mov_b64 s[8:9], 0

; #define GAS __attribute__((address_space(1)))
; #define LAS __attribute__((address_space(3)))
; __device__ __forceinline__ unsigned pk2(float lo, float hi) { return f2bf(lo) | (f2bf(hi) << 16); }
; __device__ __forceinline__ int wrow_map(int mode, int n) {
;     if (mode == 1) { if (n >= 1024 && n < 2048) { const int d = n & 63; return (n & ~63) + 32 * ((d >> 4) & 1) + 8 * ((d >> 2) & 3) + 4 * (d >> 5) + (d & 3); } return n; }
;     if (mode == 2) { if (n < DFF) return 256 * (n >> 7) + (n & 127); const int n2 = n - DFF; return 256 * (n2 >> 7) + 128 + (n2 & 127); }
;     return n;
; template <bool WT> __device__ __forceinline__ void cvt_process(const CvtItem& ci, const CvtLoad& L, LAS float* scr, int lane) {
;     ...
;     for (int j = 0; j < 4; ++j) { const int n = (lane >> 3) + 8 * j; const LAS float* s = scr + (8 * c) * 33 + n;
;         v4u o; o.x = pk2(s[0 * 33] * g0.x, s[1 * 33] * g0.y); o.y = pk2(s[2 * 33] * g0.z, s[3 * 33] * g0.w); o.z = pk2(s[4 * 33] * g1.x, s[5 * 33] * g1.y); o.w = pk2(s[6 * 33] * g1.z, s[7 * 33] * g1.w);
;         GAS v4u* dp = (GAS v4u*)(ci.WT + (size_t)(ci.row_off + wrow_map(ci.mode, n0 + n)) * ci.K + k0 + 8 * c);
;         if constexpr (WT) asm volatile("global_store_dwordx4 %0, %1, off sc1" :: "v"(dp), "v"(o) : "memory"); else if (ci.late) __builtin_nontemporal_store(o, dp); else *dp = o; }
.LBB0_628:
	s_waitcnt lgkmcnt(2)
	v_mov_b32_e32 v115, v98
	v_mov_b32_e32 v98, v85
	v_mov_b32_e32 v114, v84
	v_pk_mul_f32 v[84:85], v[90:91], v[98:99]
	s_waitcnt lgkmcnt(0)
	v_mov_b32_e32 v99, v96
	v_mov_b32_e32 v96, v95
	v_mov_b32_e32 v98, v94
	v_pk_mul_f32 v[94:95], v[86:87], v[96:97]
	v_pk_mul_f32 v[114:115], v[92:93], v[114:115]
	v_pk_mul_f32 v[98:99], v[88:89], v[98:99]
	v_cvt_pk_bf16_f32 v96, v98, v94
	v_cvt_pk_bf16_f32 v94, v114, v84
	v_add_u32_e32 v84, s19, v101
	v_cvt_pk_bf16_f32 v97, v99, v95
	v_cvt_pk_bf16_f32 v95, v115, v85
	v_ashrrev_i32_e32 v85, 31, v84
	v_mul_lo_u32 v98, s94, v85
	v_mul_lo_u32 v99, s95, v84
	v_mad_u64_u32 v[84:85], s[8:9], s94, v84, 0
	v_add3_u32 v85, v85, v98, v99
	v_lshl_add_u64 v[84:85], v[84:85], 1, s[96:97]
	v_lshl_add_u64 v[84:85], s[30:31], 1, v[84:85]
	v_lshl_add_u64 v[84:85], v[84:85], 0, v[2:3]
	global_store_dwordx4 v[84:85], v[94:97], off sc1
	ds_read2_b32 v[84:85], v135 offset0:16 offset1:49
	ds_read2_b32 v[98:99], v135 offset0:82 offset1:115
	ds_read2_b32 v[94:95], v135 offset0:148 offset1:181
	ds_read2_b32 v[96:97], v135 offset0:214 offset1:247
	v_add_u32_e32 v100, s0, v133
	s_cmp_gt_i32 s18, 1
	s_mov_b64 s[8:9], -1
	s_cbranch_scc0 .LBB0_634
	s_movk_i32 s1, 0xaff
	v_cmp_lt_i32_e32 vcc, s1, v100
	v_lshlrev_b32_e32 v114, 1, v100
	v_and_b32_e32 v113, 0x7f, v100
	s_and_saveexec_b64 s[8:9], vcc
	s_xor_b64 s[8:9], exec, s[8:9]
	v_add_u32_e32 v101, 0x7fffea00, v114
	v_and_b32_e32 v101, 0x7fffff00, v101
	s_movk_i32 s1, 0x80
	v_or3_b32 v101, v113, v101, s1
	s_andn2_saveexec_b64 s[8:9], s[8:9]
	s_movk_i32 s1, 0xff00
	v_and_or_b32 v101, v114, s1, v113
	s_or_b64 exec, exec, s[8:9]
	s_mov_b64 s[8:9], 0

; #define GAS __attribute__((address_space(1)))
; #define LAS __attribute__((address_space(3)))
; __device__ __forceinline__ unsigned pk2(float lo, float hi) { return f2bf(lo) | (f2bf(hi) << 16); }
; __device__ __forceinline__ int wrow_map(int mode, int n) {
;     if (mode == 1) { if (n >= 1024 && n < 2048) { const int d = n & 63; return (n & ~63) + 32 * ((d >> 4) & 1) + 8 * ((d >> 2) & 3) + 4 * (d >> 5) + (d & 3); } return n; }
;     if (mode == 2) { if (n < DFF) return 256 * (n >> 7) + (n & 127); const int n2 = n - DFF; return 256 * (n2 >> 7) + 128 + (n2 & 127); }
;     return n;
; template <bool WT> __device__ __forceinline__ void cvt_process(const CvtItem& ci, const CvtLoad& L, LAS float* scr, int lane) {
;     ...
;     for (int j = 0; j < 4; ++j) { const int n = (lane >> 3) + 8 * j; const LAS float* s = scr + (8 * c) * 33 + n;
;         v4u o; o.x = pk2(s[0 * 33] * g0.x, s[1 * 33] * g0.y); o.y = pk2(s[2 * 33] * g0.z, s[3 * 33] * g0.w); o.z = pk2(s[4 * 33] * g1.x, s[5 * 33] * g1.y); o.w = pk2(s[6 * 33] * g1.z, s[7 * 33] * g1.w);
;         GAS v4u* dp = (GAS v4u*)(ci.WT + (size_t)(ci.row_off + wrow_map(ci.mode, n0 + n)) * ci.K + k0 + 8 * c);
;         if constexpr (WT) asm volatile("global_store_dwordx4 %0, %1, off sc1" :: "v"(dp), "v"(o) : "memory"); else if (ci.late) __builtin_nontemporal_store(o, dp); else *dp = o; }
.LBB0_638:
	s_waitcnt lgkmcnt(2)
	v_mov_b32_e32 v115, v98
	v_mov_b32_e32 v98, v85
	v_mov_b32_e32 v114, v84
	v_pk_mul_f32 v[84:85], v[90:91], v[98:99]
	s_waitcnt lgkmcnt(0)
	v_mov_b32_e32 v99, v96
	v_mov_b32_e32 v96, v95
	v_mov_b32_e32 v98, v94
	v_pk_mul_f32 v[94:95], v[86:87], v[96:97]
	v_pk_mul_f32 v[114:115], v[92:93], v[114:115]
	v_pk_mul_f32 v[98:99], v[88:89], v[98:99]
	v_cvt_pk_bf16_f32 v96, v98, v94
	v_cvt_pk_bf16_f32 v94, v114, v84
	v_add_u32_e32 v84, s19, v101
	v_cvt_pk_bf16_f32 v97, v99, v95
	v_cvt_pk_bf16_f32 v95, v115, v85
	v_ashrrev_i32_e32 v85, 31, v84
	v_mul_lo_u32 v98, s94, v85
	v_mul_lo_u32 v99, s95, v84
	v_mad_u64_u32 v[84:85], s[8:9], s94, v84, 0
	v_add3_u32 v85, v85, v98, v99
	v_lshl_add_u64 v[84:85], v[84:85], 1, s[96:97]
	v_lshl_add_u64 v[84:85], s[30:31], 1, v[84:85]
	v_lshl_add_u64 v[84:85], v[84:85], 0, v[2:3]
	global_store_dwordx4 v[84:85], v[94:97], off sc1
	ds_read2_b32 v[94:95], v135 offset0:24 offset1:57
	ds_read2_b32 v[96:97], v135 offset0:90 offset1:123
	ds_read2_b32 v[84:85], v135 offset0:156 offset1:189
	ds_read2_b32 v[100:101], v135 offset0:222 offset1:255
	s_cmp_gt_i32 s18, 1
	s_waitcnt lgkmcnt(3)
	v_mov_b32_e32 v98, v95
	s_waitcnt lgkmcnt(2)
	v_mov_b32_e32 v95, v96
	v_mov_b32_e32 v99, v97
	s_waitcnt lgkmcnt(1)
	v_mov_b32_e32 v96, v85
	s_waitcnt lgkmcnt(0)
	v_mov_b32_e32 v85, v100
	v_mov_b32_e32 v97, v101
	v_add_u32_e32 v101, s0, v134
	s_mov_b64 s[0:1], -1
	s_cbranch_scc0 .LBB0_644
	s_movk_i32 s0, 0xaff
	v_cmp_lt_i32_e32 vcc, s0, v101
	v_lshlrev_b32_e32 v114, 1, v101
	v_and_b32_e32 v113, 0x7f, v101
	s_and_saveexec_b64 s[0:1], vcc
	s_xor_b64 s[0:1], exec, s[0:1]
	v_add_u32_e32 v100, 0x7fffea00, v114
	v_and_b32_e32 v100, 0x7fffff00, v100
	s_movk_i32 s8, 0x80
	v_or3_b32 v100, v113, v100, s8
	s_andn2_saveexec_b64 s[0:1], s[0:1]
	s_movk_i32 s8, 0xff00
	v_and_or_b32 v100, v114, s8, v113
	s_or_b64 exec, exec, s[0:1]
	s_mov_b64 s[0:1], 0

; #define GAS __attribute__((address_space(1)))
; #define LAS __attribute__((address_space(3)))
; #define LDS_WAIT() asm volatile("s_waitcnt lgkmcnt(0)" ::: "memory")
; __device__ __forceinline__ unsigned pk2(float lo, float hi) { return f2bf(lo) | (f2bf(hi) << 16); }
; template <bool WT> __device__ __forceinline__ void cvt_process(const CvtItem& ci, const CvtLoad& L, LAS float* scr, int lane) {
;     ...
;     for (int j = 0; j < 4; ++j) { const int n = (lane >> 3) + 8 * j; const LAS float* s = scr + (8 * c) * 33 + n;
;         v4u o; o.x = pk2(s[0 * 33] * g0.x, s[1 * 33] * g0.y); o.y = pk2(s[2 * 33] * g0.z, s[3 * 33] * g0.w); o.z = pk2(s[4 * 33] * g1.x, s[5 * 33] * g1.y); o.w = pk2(s[6 * 33] * g1.z, s[7 * 33] * g1.w);
;         GAS v4u* dp = (GAS v4u*)(ci.WT + (size_t)(ci.row_off + wrow_map(ci.mode, n0 + n)) * ci.K + k0 + 8 * c);
;         if constexpr (WT) asm volatile("global_store_dwordx4 %0, %1, off sc1" :: "v"(dp), "v"(o) : "memory"); else if (ci.late) __builtin_nontemporal_store(o, dp); else *dp = o; }
;     LDS_WAIT(); asm volatile("" ::: "memory");
.LBB0_648:
	v_pk_mul_f32 v[90:91], v[90:91], v[98:99]
	v_pk_mul_f32 v[86:87], v[86:87], v[96:97]
	v_pk_mul_f32 v[92:93], v[92:93], v[94:95]
	v_pk_mul_f32 v[84:85], v[88:89], v[84:85]
	v_cvt_pk_bf16_f32 v86, v84, v86
	v_cvt_pk_bf16_f32 v84, v92, v90
	v_add_u32_e32 v88, s19, v100
	v_cvt_pk_bf16_f32 v87, v85, v87
	v_cvt_pk_bf16_f32 v85, v93, v91
	v_ashrrev_i32_e32 v89, 31, v88
	v_mul_lo_u32 v90, s94, v89
	v_mul_lo_u32 v91, s95, v88
	v_mad_u64_u32 v[88:89], s[0:1], s94, v88, 0
	v_add3_u32 v89, v89, v90, v91
	v_lshl_add_u64 v[88:89], v[88:89], 1, s[96:97]
	v_lshl_add_u64 v[88:89], s[30:31], 1, v[88:89]
	v_lshl_add_u64 v[88:89], v[88:89], 0, v[2:3]
	global_store_dwordx4 v[88:89], v[84:87], off sc1
	s_waitcnt lgkmcnt(0)
	s_andn2_b64 vcc, exec, s[26:27]
	s_cbranch_vccz .LBB0_650
	s_andn2_b64 vcc, exec, s[20:21]
	s_cbranch_vccnz .LBB0_553
	s_branch .LBB0_691

; #define GAS __attribute__((address_space(1)))
; #define LAS __attribute__((address_space(3)))
; #define LDS_WAIT() asm volatile("s_waitcnt lgkmcnt(0)" ::: "memory")
; __device__ __forceinline__ unsigned pk2(float lo, float hi) { return f2bf(lo) | (f2bf(hi) << 16); }
; __device__ __forceinline__ int wrow_map(int mode, int n) {
;     if (mode == 1) { if (n >= 1024 && n < 2048) { const int d = n & 63; return (n & ~63) + 32 * ((d >> 4) & 1) + 8 * ((d >> 2) & 3) + 4 * (d >> 5) + (d & 3); } return n; }
;     if (mode == 2) { if (n < DFF) return 256 * (n >> 7) + (n & 127); const int n2 = n - DFF; return 256 * (n2 >> 7) + 128 + (n2 & 127); }
;     return n;
; template <bool WT> __device__ __forceinline__ void cvt_process(const CvtItem& ci, const CvtLoad& L, LAS float* scr, int lane) {
;     ...
;     const int c = lane & 7; const bool hg = ci.gk != nullptr;
;     f32x4 g0, g1;
; #pragma unroll
;     for (int e = 0; e < 4; ++e) { g0[e] = hg ? L.g0[e] : 1.f; g1[e] = hg ? L.g1[e] : 1.f; }
;     LDS_WAIT(); asm volatile("" ::: "memory");
; #pragma unroll
;     for (int j = 0; j < 4; ++j) { const int n = (lane >> 3) + 8 * j; const LAS float* s = scr + (8 * c) * 33 + n;
;         v4u o; o.x = pk2(s[0 * 33] * g0.x, s[1 * 33] * g0.y); o.y = pk2(s[2 * 33] * g0.z, s[3 * 33] * g0.w); o.z = pk2(s[4 * 33] * g1.x, s[5 * 33] * g1.y); o.w = pk2(s[6 * 33] * g1.z, s[7 * 33] * g1.w);
;         GAS v4u* dp = (GAS v4u*)(ci.WT + (size_t)(ci.row_off + wrow_map(ci.mode, n0 + n)) * ci.K + k0 + 8 * c);
;         if constexpr (WT) asm volatile("global_store_dwordx4 %0, %1, off sc1" :: "v"(dp), "v"(o) : "memory"); else if (ci.late) __builtin_nontemporal_store(o, dp); else *dp = o; }
.LBB0_660:
	v_cndmask_b32_e64 v53, v50, 1.0, s[6:7]
	v_cndmask_b32_e64 v51, v51, 1.0, s[6:7]
	v_cndmask_b32_e64 v50, v49, 1.0, s[6:7]
	v_cndmask_b32_e64 v49, v46, 1.0, s[6:7]
	v_cndmask_b32_e64 v46, v45, 1.0, s[6:7]
	s_waitcnt lgkmcnt(2)
	v_mov_b32_e32 v45, v60
	v_mov_b32_e32 v60, v55
	v_cndmask_b32_e64 v52, v48, 1.0, s[6:7]
	v_cndmask_b32_e64 v48, v44, 1.0, s[6:7]
	v_cndmask_b32_e64 v47, v47, 1.0, s[6:7]
	v_mov_b32_e32 v44, v54
	v_pk_mul_f32 v[54:55], v[50:51], v[60:61]
	s_waitcnt lgkmcnt(0)
	v_mov_b32_e32 v61, v58
	v_mov_b32_e32 v58, v57
	v_mov_b32_e32 v60, v56
	v_pk_mul_f32 v[56:57], v[46:47], v[58:59]
	v_pk_mul_f32 v[44:45], v[52:53], v[44:45]
	v_pk_mul_f32 v[60:61], v[48:49], v[60:61]
	v_cvt_pk_bf16_f32 v54, v44, v54
	v_add_u32_e32 v44, s11, v62
	v_cvt_pk_bf16_f32 v55, v45, v55
	v_ashrrev_i32_e32 v45, 31, v44
	v_cvt_pk_bf16_f32 v57, v61, v57
	v_cvt_pk_bf16_f32 v56, v60, v56
	v_mul_lo_u32 v58, s90, v45
	v_mul_lo_u32 v59, s91, v44
	v_mad_u64_u32 v[44:45], s[0:1], s90, v44, 0
	v_add3_u32 v45, v45, v58, v59
	v_lshl_add_u64 v[44:45], v[44:45], 1, s[92:93]
	v_lshl_add_u64 v[44:45], s[40:41], 1, v[44:45]
	v_lshl_add_u64 v[44:45], v[44:45], 0, v[2:3]
	global_store_dwordx4 v[44:45], v[54:57], off sc1
	ds_read2_b32 v[44:45], v135 offset0:8 offset1:41
	ds_read2_b32 v[58:59], v135 offset0:74 offset1:107
	ds_read2_b32 v[54:55], v135 offset0:140 offset1:173
	ds_read2_b32 v[56:57], v135 offset0:206 offset1:239
	v_add_u32_e32 v61, s28, v132
	s_cmp_gt_i32 s10, 1
	s_mov_b64 s[0:1], -1
	s_cbranch_scc0 .LBB0_666
	s_movk_i32 s0, 0xaff
	v_cmp_lt_i32_e32 vcc, s0, v61
	v_lshlrev_b32_e32 v63, 1, v61
	v_and_b32_e32 v62, 0x7f, v61
	s_and_saveexec_b64 s[0:1], vcc
	s_xor_b64 s[0:1], exec, s[0:1]
	v_add_u32_e32 v60, 0x7fffea00, v63
	v_and_b32_e32 v60, 0x7fffff00, v60
	s_movk_i32 s6, 0x80
	v_or3_b32 v60, v62, v60, s6
	s_andn2_saveexec_b64 s[0:1], s[0:1]
	s_movk_i32 s6, 0xff00
	v_and_or_b32 v60, v63, s6, v62
	s_or_b64 exec, exec, s[0:1]
	s_mov_b64 s[0:1], 0

; #define GAS __attribute__((address_space(1)))
; #define LAS __attribute__((address_space(3)))
; __device__ __forceinline__ unsigned pk2(float lo, float hi) { return f2bf(lo) | (f2bf(hi) << 16); }
; __device__ __forceinline__ int wrow_map(int mode, int n) {
;     if (mode == 1) { if (n >= 1024 && n < 2048) { const int d = n & 63; return (n & ~63) + 32 * ((d >> 4) & 1) + 8 * ((d >> 2) & 3) + 4 * (d >> 5) + (d & 3); } return n; }
;     if (mode == 2) { if (n < DFF) return 256 * (n >> 7) + (n & 127); const int n2 = n - DFF; return 256 * (n2 >> 7) + 128 + (n2 & 127); }
;     return n;
; template <bool WT> __device__ __forceinline__ void cvt_process(const CvtItem& ci, const CvtLoad& L, LAS float* scr, int lane) {
;     ...
;     for (int j = 0; j < 4; ++j) { const int n = (lane >> 3) + 8 * j; const LAS float* s = scr + (8 * c) * 33 + n;
;         v4u o; o.x = pk2(s[0 * 33] * g0.x, s[1 * 33] * g0.y); o.y = pk2(s[2 * 33] * g0.z, s[3 * 33] * g0.w); o.z = pk2(s[4 * 33] * g1.x, s[5 * 33] * g1.y); o.w = pk2(s[6 * 33] * g1.z, s[7 * 33] * g1.w);
;         GAS v4u* dp = (GAS v4u*)(ci.WT + (size_t)(ci.row_off + wrow_map(ci.mode, n0 + n)) * ci.K + k0 + 8 * c);
;         if constexpr (WT) asm volatile("global_store_dwordx4 %0, %1, off sc1" :: "v"(dp), "v"(o) : "memory"); else if (ci.late) __builtin_nontemporal_store(o, dp); else *dp = o; }
.LBB0_670:
	s_waitcnt lgkmcnt(2)
	v_mov_b32_e32 v63, v58
	v_mov_b32_e32 v58, v45
	v_mov_b32_e32 v62, v44
	v_pk_mul_f32 v[44:45], v[50:51], v[58:59]
	s_waitcnt lgkmcnt(0)
	v_mov_b32_e32 v59, v56
	v_mov_b32_e32 v56, v55
	v_mov_b32_e32 v58, v54
	v_pk_mul_f32 v[54:55], v[46:47], v[56:57]
	v_pk_mul_f32 v[62:63], v[52:53], v[62:63]
	v_pk_mul_f32 v[58:59], v[48:49], v[58:59]
	v_cvt_pk_bf16_f32 v56, v58, v54
	v_cvt_pk_bf16_f32 v54, v62, v44
	v_add_u32_e32 v44, s11, v60
	v_cvt_pk_bf16_f32 v57, v59, v55
	v_cvt_pk_bf16_f32 v55, v63, v45
	v_ashrrev_i32_e32 v45, 31, v44
	v_mul_lo_u32 v58, s90, v45
	v_mul_lo_u32 v59, s91, v44
	v_mad_u64_u32 v[44:45], s[0:1], s90, v44, 0
	v_add3_u32 v45, v45, v58, v59
	v_lshl_add_u64 v[44:45], v[44:45], 1, s[92:93]
	v_lshl_add_u64 v[44:45], s[40:41], 1, v[44:45]
	v_lshl_add_u64 v[44:45], v[44:45], 0, v[2:3]
	global_store_dwordx4 v[44:45], v[54:57], off sc1
	ds_read2_b32 v[44:45], v135 offset0:16 offset1:49
	ds_read2_b32 v[58:59], v135 offset0:82 offset1:115
	ds_read2_b32 v[54:55], v135 offset0:148 offset1:181
	ds_read2_b32 v[56:57], v135 offset0:214 offset1:247
	v_add_u32_e32 v61, s28, v133
	s_cmp_gt_i32 s10, 1
	s_mov_b64 s[0:1], -1
	s_cbranch_scc0 .LBB0_676
	s_movk_i32 s0, 0xaff
	v_cmp_lt_i32_e32 vcc, s0, v61
	v_lshlrev_b32_e32 v63, 1, v61
	v_and_b32_e32 v62, 0x7f, v61
	s_and_saveexec_b64 s[0:1], vcc
	s_xor_b64 s[0:1], exec, s[0:1]
	v_add_u32_e32 v60, 0x7fffea00, v63
	v_and_b32_e32 v60, 0x7fffff00, v60
	s_movk_i32 s6, 0x80
	v_or3_b32 v60, v62, v60, s6
	s_andn2_saveexec_b64 s[0:1], s[0:1]
	s_movk_i32 s6, 0xff00
	v_and_or_b32 v60, v63, s6, v62
	s_or_b64 exec, exec, s[0:1]
	s_mov_b64 s[0:1], 0

; #define GAS __attribute__((address_space(1)))
; #define LAS __attribute__((address_space(3)))
; __device__ __forceinline__ unsigned pk2(float lo, float hi) { return f2bf(lo) | (f2bf(hi) << 16); }
; __device__ __forceinline__ int wrow_map(int mode, int n) {
;     if (mode == 1) { if (n >= 1024 && n < 2048) { const int d = n & 63; return (n & ~63) + 32 * ((d >> 4) & 1) + 8 * ((d >> 2) & 3) + 4 * (d >> 5) + (d & 3); } return n; }
;     if (mode == 2) { if (n < DFF) return 256 * (n >> 7) + (n & 127); const int n2 = n - DFF; return 256 * (n2 >> 7) + 128 + (n2 & 127); }
;     return n;
; template <bool WT> __device__ __forceinline__ void cvt_process(const CvtItem& ci, const CvtLoad& L, LAS float* scr, int lane) {
;     ...
;     for (int j = 0; j < 4; ++j) { const int n = (lane >> 3) + 8 * j; const LAS float* s = scr + (8 * c) * 33 + n;
;         v4u o; o.x = pk2(s[0 * 33] * g0.x, s[1 * 33] * g0.y); o.y = pk2(s[2 * 33] * g0.z, s[3 * 33] * g0.w); o.z = pk2(s[4 * 33] * g1.x, s[5 * 33] * g1.y); o.w = pk2(s[6 * 33] * g1.z, s[7 * 33] * g1.w);
;         GAS v4u* dp = (GAS v4u*)(ci.WT + (size_t)(ci.row_off + wrow_map(ci.mode, n0 + n)) * ci.K + k0 + 8 * c);
;         if constexpr (WT) asm volatile("global_store_dwordx4 %0, %1, off sc1" :: "v"(dp), "v"(o) : "memory"); else if (ci.late) __builtin_nontemporal_store(o, dp); else *dp = o; }
.LBB0_680:
	s_waitcnt lgkmcnt(2)
	v_mov_b32_e32 v63, v58
	v_mov_b32_e32 v58, v45
	v_mov_b32_e32 v62, v44
	v_pk_mul_f32 v[44:45], v[50:51], v[58:59]
	s_waitcnt lgkmcnt(0)
	v_mov_b32_e32 v59, v56
	v_mov_b32_e32 v56, v55
	v_mov_b32_e32 v58, v54
	v_pk_mul_f32 v[54:55], v[46:47], v[56:57]
	v_pk_mul_f32 v[62:63], v[52:53], v[62:63]
	v_pk_mul_f32 v[58:59], v[48:49], v[58:59]
	v_cvt_pk_bf16_f32 v56, v58, v54
	v_cvt_pk_bf16_f32 v54, v62, v44
	v_add_u32_e32 v44, s11, v60
	v_cvt_pk_bf16_f32 v57, v59, v55
	v_cvt_pk_bf16_f32 v55, v63, v45
	v_ashrrev_i32_e32 v45, 31, v44
	v_mul_lo_u32 v58, s90, v45
	v_mul_lo_u32 v59, s91, v44
	v_mad_u64_u32 v[44:45], s[0:1], s90, v44, 0
	v_add3_u32 v45, v45, v58, v59
	v_lshl_add_u64 v[44:45], v[44:45], 1, s[92:93]
	v_lshl_add_u64 v[44:45], s[40:41], 1, v[44:45]
	v_lshl_add_u64 v[44:45], v[44:45], 0, v[2:3]
	global_store_dwordx4 v[44:45], v[54:57], off sc1
	ds_read2_b32 v[54:55], v135 offset0:24 offset1:57
	ds_read2_b32 v[56:57], v135 offset0:90 offset1:123
	ds_read2_b32 v[44:45], v135 offset0:156 offset1:189
	ds_read2_b32 v[58:59], v135 offset0:222 offset1:255
	v_add_u32_e32 v61, s28, v134
	s_cmp_gt_i32 s10, 1
	s_mov_b64 s[0:1], -1
	s_cbranch_scc0 .LBB0_686
	s_movk_i32 s0, 0xaff
	v_cmp_lt_i32_e32 vcc, s0, v61
	v_lshlrev_b32_e32 v63, 1, v61
	v_and_b32_e32 v62, 0x7f, v61
	s_and_saveexec_b64 s[0:1], vcc
	s_xor_b64 s[0:1], exec, s[0:1]
	v_add_u32_e32 v60, 0x7fffea00, v63
	v_and_b32_e32 v60, 0x7fffff00, v60
	s_movk_i32 s6, 0x80
	v_or3_b32 v60, v62, v60, s6
	s_andn2_saveexec_b64 s[0:1], s[0:1]
	s_movk_i32 s6, 0xff00
	v_and_or_b32 v60, v63, s6, v62
	s_or_b64 exec, exec, s[0:1]
	s_mov_b64 s[0:1], 0

; #define GAS __attribute__((address_space(1)))
; #define LAS __attribute__((address_space(3)))
; #define LDS_WAIT() asm volatile("s_waitcnt lgkmcnt(0)" ::: "memory")
; __device__ __forceinline__ unsigned pk2(float lo, float hi) { return f2bf(lo) | (f2bf(hi) << 16); }
; template <bool WT> __device__ __forceinline__ void cvt_process(const CvtItem& ci, const CvtLoad& L, LAS float* scr, int lane) {
;     ...
;     for (int j = 0; j < 4; ++j) { const int n = (lane >> 3) + 8 * j; const LAS float* s = scr + (8 * c) * 33 + n;
;         v4u o; o.x = pk2(s[0 * 33] * g0.x, s[1 * 33] * g0.y); o.y = pk2(s[2 * 33] * g0.z, s[3 * 33] * g0.w); o.z = pk2(s[4 * 33] * g1.x, s[5 * 33] * g1.y); o.w = pk2(s[6 * 33] * g1.z, s[7 * 33] * g1.w);
;         GAS v4u* dp = (GAS v4u*)(ci.WT + (size_t)(ci.row_off + wrow_map(ci.mode, n0 + n)) * ci.K + k0 + 8 * c);
;         if constexpr (WT) asm volatile("global_store_dwordx4 %0, %1, off sc1" :: "v"(dp), "v"(o) : "memory"); else if (ci.late) __builtin_nontemporal_store(o, dp); else *dp = o; }
;     LDS_WAIT(); asm volatile("" ::: "memory");
.LBB0_690:
	s_waitcnt lgkmcnt(3)
	v_mov_b32_e32 v62, v55
	s_waitcnt lgkmcnt(2)
	v_mov_b32_e32 v55, v56
	v_mov_b32_e32 v63, v57
	v_pk_mul_f32 v[52:53], v[52:53], v[54:55]
	s_waitcnt lgkmcnt(1)
	v_mov_b32_e32 v54, v45
	s_waitcnt lgkmcnt(0)
	v_mov_b32_e32 v55, v59
	v_pk_mul_f32 v[50:51], v[50:51], v[62:63]
	v_pk_mul_f32 v[46:47], v[46:47], v[54:55]
	v_mov_b32_e32 v45, v58
	v_pk_mul_f32 v[44:45], v[48:49], v[44:45]
	v_cvt_pk_bf16_f32 v46, v44, v46
	v_cvt_pk_bf16_f32 v44, v52, v50
	v_add_u32_e32 v48, s11, v60
	v_cvt_pk_bf16_f32 v47, v45, v47
	v_cvt_pk_bf16_f32 v45, v53, v51
	v_ashrrev_i32_e32 v49, 31, v48
	v_mul_lo_u32 v50, s90, v49
	v_mul_lo_u32 v51, s91, v48
	v_mad_u64_u32 v[48:49], s[0:1], s90, v48, 0
	v_add3_u32 v49, v49, v50, v51
	v_lshl_add_u64 v[48:49], v[48:49], 1, s[92:93]
	v_lshl_add_u64 v[48:49], s[40:41], 1, v[48:49]
	v_lshl_add_u64 v[48:49], v[48:49], 0, v[2:3]
	global_store_dwordx4 v[48:49], v[44:47], off sc1
	s_waitcnt lgkmcnt(0)
	s_andn2_b64 vcc, exec, s[20:21]
	s_cbranch_vccnz .LBB0_553

; #define GAS __attribute__((address_space(1)))
; #define LAS __attribute__((address_space(3)))
; #define LDS_WAIT() asm volatile("s_waitcnt lgkmcnt(0)" ::: "memory")
; __device__ __forceinline__ unsigned pk2(float lo, float hi) { return f2bf(lo) | (f2bf(hi) << 16); }
; __device__ __forceinline__ int wrow_map(int mode, int n) {
;     if (mode == 1) { if (n >= 1024 && n < 2048) { const int d = n & 63; return (n & ~63) + 32 * ((d >> 4) & 1) + 8 * ((d >> 2) & 3) + 4 * (d >> 5) + (d & 3); } return n; }
;     if (mode == 2) { if (n < DFF) return 256 * (n >> 7) + (n & 127); const int n2 = n - DFF; return 256 * (n2 >> 7) + 128 + (n2 & 127); }
;     return n;
; template <bool WT> __device__ __forceinline__ void cvt_process(const CvtItem& ci, const CvtLoad& L, LAS float* scr, int lane) {
;     ...
;     const int c = lane & 7; const bool hg = ci.gk != nullptr;
;     f32x4 g0, g1;
; #pragma unroll
;     for (int e = 0; e < 4; ++e) { g0[e] = hg ? L.g0[e] : 1.f; g1[e] = hg ? L.g1[e] : 1.f; }
;     LDS_WAIT(); asm volatile("" ::: "memory");
; #pragma unroll
;     for (int j = 0; j < 4; ++j) { const int n = (lane >> 3) + 8 * j; const LAS float* s = scr + (8 * c) * 33 + n;
;         v4u o; o.x = pk2(s[0 * 33] * g0.x, s[1 * 33] * g0.y); o.y = pk2(s[2 * 33] * g0.z, s[3 * 33] * g0.w); o.z = pk2(s[4 * 33] * g1.x, s[5 * 33] * g1.y); o.w = pk2(s[6 * 33] * g1.z, s[7 * 33] * g1.w);
;         GAS v4u* dp = (GAS v4u*)(ci.WT + (size_t)(ci.row_off + wrow_map(ci.mode, n0 + n)) * ci.K + k0 + 8 * c);
;         if constexpr (WT) asm volatile("global_store_dwordx4 %0, %1, off sc1" :: "v"(dp), "v"(o) : "memory"); else if (ci.late) __builtin_nontemporal_store(o, dp); else *dp = o; }
.LBB0_701:
	v_cndmask_b32_e64 v13, v10, 1.0, s[4:5]
	v_cndmask_b32_e64 v11, v11, 1.0, s[4:5]
	v_cndmask_b32_e64 v10, v9, 1.0, s[4:5]
	v_cndmask_b32_e64 v9, v6, 1.0, s[4:5]
	v_cndmask_b32_e64 v6, v5, 1.0, s[4:5]
	s_waitcnt lgkmcnt(2)
	v_mov_b32_e32 v5, v20
	v_mov_b32_e32 v20, v15
	v_cndmask_b32_e64 v12, v8, 1.0, s[4:5]
	v_cndmask_b32_e64 v8, v4, 1.0, s[4:5]
	v_cndmask_b32_e64 v7, v7, 1.0, s[4:5]
	v_mov_b32_e32 v4, v14
	v_pk_mul_f32 v[14:15], v[10:11], v[20:21]
	s_waitcnt lgkmcnt(0)
	v_mov_b32_e32 v21, v18
	v_mov_b32_e32 v18, v17
	v_mov_b32_e32 v20, v16
	v_pk_mul_f32 v[16:17], v[6:7], v[18:19]
	v_pk_mul_f32 v[4:5], v[12:13], v[4:5]
	v_pk_mul_f32 v[20:21], v[8:9], v[20:21]
	v_cvt_pk_bf16_f32 v14, v4, v14
	v_add_u32_e32 v4, s23, v22
	v_cvt_pk_bf16_f32 v15, v5, v15
	v_ashrrev_i32_e32 v5, 31, v4
	v_cvt_pk_bf16_f32 v17, v21, v17
	v_cvt_pk_bf16_f32 v16, v20, v16
	v_mul_lo_u32 v18, s86, v5
	v_mul_lo_u32 v19, s87, v4
	v_mad_u64_u32 v[4:5], s[0:1], s86, v4, 0
	v_add3_u32 v5, v5, v18, v19
	v_lshl_add_u64 v[4:5], v[4:5], 1, s[88:89]
	v_lshl_add_u64 v[4:5], s[34:35], 1, v[4:5]
	v_lshl_add_u64 v[4:5], v[4:5], 0, v[2:3]
	global_store_dwordx4 v[4:5], v[14:17], off sc1
	ds_read2_b32 v[4:5], v135 offset0:8 offset1:41
	ds_read2_b32 v[18:19], v135 offset0:74 offset1:107
	ds_read2_b32 v[14:15], v135 offset0:140 offset1:173
	ds_read2_b32 v[16:17], v135 offset0:206 offset1:239
	v_add_u32_e32 v21, s14, v132
	s_cmp_gt_i32 s22, 1
	s_mov_b64 s[0:1], -1
	s_cbranch_scc0 .LBB0_707
	s_movk_i32 s0, 0xaff
	v_cmp_lt_i32_e32 vcc, s0, v21
	v_lshlrev_b32_e32 v23, 1, v21
	v_and_b32_e32 v22, 0x7f, v21
	s_and_saveexec_b64 s[0:1], vcc
	s_xor_b64 s[0:1], exec, s[0:1]
	v_add_u32_e32 v20, 0x7fffea00, v23
	v_and_b32_e32 v20, 0x7fffff00, v20
	s_movk_i32 s4, 0x80
	v_or3_b32 v20, v22, v20, s4
	s_andn2_saveexec_b64 s[0:1], s[0:1]
	s_movk_i32 s4, 0xff00
	v_and_or_b32 v20, v23, s4, v22
	s_or_b64 exec, exec, s[0:1]
	s_mov_b64 s[0:1], 0

; #define GAS __attribute__((address_space(1)))
; #define LAS __attribute__((address_space(3)))
; __device__ __forceinline__ unsigned pk2(float lo, float hi) { return f2bf(lo) | (f2bf(hi) << 16); }
; __device__ __forceinline__ int wrow_map(int mode, int n) {
;     if (mode == 1) { if (n >= 1024 && n < 2048) { const int d = n & 63; return (n & ~63) + 32 * ((d >> 4) & 1) + 8 * ((d >> 2) & 3) + 4 * (d >> 5) + (d & 3); } return n; }
;     if (mode == 2) { if (n < DFF) return 256 * (n >> 7) + (n & 127); const int n2 = n - DFF; return 256 * (n2 >> 7) + 128 + (n2 & 127); }
;     return n;
; template <bool WT> __device__ __forceinline__ void cvt_process(const CvtItem& ci, const CvtLoad& L, LAS float* scr, int lane) {
;     ...
;     for (int j = 0; j < 4; ++j) { const int n = (lane >> 3) + 8 * j; const LAS float* s = scr + (8 * c) * 33 + n;
;         v4u o; o.x = pk2(s[0 * 33] * g0.x, s[1 * 33] * g0.y); o.y = pk2(s[2 * 33] * g0.z, s[3 * 33] * g0.w); o.z = pk2(s[4 * 33] * g1.x, s[5 * 33] * g1.y); o.w = pk2(s[6 * 33] * g1.z, s[7 * 33] * g1.w);
;         GAS v4u* dp = (GAS v4u*)(ci.WT + (size_t)(ci.row_off + wrow_map(ci.mode, n0 + n)) * ci.K + k0 + 8 * c);
;         if constexpr (WT) asm volatile("global_store_dwordx4 %0, %1, off sc1" :: "v"(dp), "v"(o) : "memory"); else if (ci.late) __builtin_nontemporal_store(o, dp); else *dp = o; }
.LBB0_711:
	s_waitcnt lgkmcnt(2)
	v_mov_b32_e32 v23, v18
	v_mov_b32_e32 v18, v5
	v_mov_b32_e32 v22, v4
	v_pk_mul_f32 v[4:5], v[10:11], v[18:19]
	s_waitcnt lgkmcnt(0)
	v_mov_b32_e32 v19, v16
	v_mov_b32_e32 v16, v15
	v_mov_b32_e32 v18, v14
	v_pk_mul_f32 v[14:15], v[6:7], v[16:17]
	v_pk_mul_f32 v[22:23], v[12:13], v[22:23]
	v_pk_mul_f32 v[18:19], v[8:9], v[18:19]
	v_cvt_pk_bf16_f32 v16, v18, v14
	v_cvt_pk_bf16_f32 v14, v22, v4
	v_add_u32_e32 v4, s23, v20
	v_cvt_pk_bf16_f32 v17, v19, v15
	v_cvt_pk_bf16_f32 v15, v23, v5
	v_ashrrev_i32_e32 v5, 31, v4
	v_mul_lo_u32 v18, s86, v5
	v_mul_lo_u32 v19, s87, v4
	v_mad_u64_u32 v[4:5], s[0:1], s86, v4, 0
	v_add3_u32 v5, v5, v18, v19
	v_lshl_add_u64 v[4:5], v[4:5], 1, s[88:89]
	v_lshl_add_u64 v[4:5], s[34:35], 1, v[4:5]
	v_lshl_add_u64 v[4:5], v[4:5], 0, v[2:3]
	global_store_dwordx4 v[4:5], v[14:17], off sc1
	ds_read2_b32 v[4:5], v135 offset0:16 offset1:49
	ds_read2_b32 v[18:19], v135 offset0:82 offset1:115
	ds_read2_b32 v[14:15], v135 offset0:148 offset1:181
	ds_read2_b32 v[16:17], v135 offset0:214 offset1:247
	v_add_u32_e32 v21, s14, v133
	s_cmp_gt_i32 s22, 1
	s_mov_b64 s[0:1], -1
	s_cbranch_scc0 .LBB0_717
	s_movk_i32 s0, 0xaff
	v_cmp_lt_i32_e32 vcc, s0, v21
	v_lshlrev_b32_e32 v23, 1, v21
	v_and_b32_e32 v22, 0x7f, v21
	s_and_saveexec_b64 s[0:1], vcc
	s_xor_b64 s[0:1], exec, s[0:1]
	v_add_u32_e32 v20, 0x7fffea00, v23
	v_and_b32_e32 v20, 0x7fffff00, v20
	s_movk_i32 s4, 0x80
	v_or3_b32 v20, v22, v20, s4
	s_andn2_saveexec_b64 s[0:1], s[0:1]
	s_movk_i32 s4, 0xff00
	v_and_or_b32 v20, v23, s4, v22
	s_or_b64 exec, exec, s[0:1]
	s_mov_b64 s[0:1], 0

; #define GAS __attribute__((address_space(1)))
; #define LAS __attribute__((address_space(3)))
; __device__ __forceinline__ unsigned pk2(float lo, float hi) { return f2bf(lo) | (f2bf(hi) << 16); }
; __device__ __forceinline__ int wrow_map(int mode, int n) {
;     if (mode == 1) { if (n >= 1024 && n < 2048) { const int d = n & 63; return (n & ~63) + 32 * ((d >> 4) & 1) + 8 * ((d >> 2) & 3) + 4 * (d >> 5) + (d & 3); } return n; }
;     if (mode == 2) { if (n < DFF) return 256 * (n >> 7) + (n & 127); const int n2 = n - DFF; return 256 * (n2 >> 7) + 128 + (n2 & 127); }
;     return n;
; template <bool WT> __device__ __forceinline__ void cvt_process(const CvtItem& ci, const CvtLoad& L, LAS float* scr, int lane) {
;     ...
;     for (int j = 0; j < 4; ++j) { const int n = (lane >> 3) + 8 * j; const LAS float* s = scr + (8 * c) * 33 + n;
;         v4u o; o.x = pk2(s[0 * 33] * g0.x, s[1 * 33] * g0.y); o.y = pk2(s[2 * 33] * g0.z, s[3 * 33] * g0.w); o.z = pk2(s[4 * 33] * g1.x, s[5 * 33] * g1.y); o.w = pk2(s[6 * 33] * g1.z, s[7 * 33] * g1.w);
;         GAS v4u* dp = (GAS v4u*)(ci.WT + (size_t)(ci.row_off + wrow_map(ci.mode, n0 + n)) * ci.K + k0 + 8 * c);
;         if constexpr (WT) asm volatile("global_store_dwordx4 %0, %1, off sc1" :: "v"(dp), "v"(o) : "memory"); else if (ci.late) __builtin_nontemporal_store(o, dp); else *dp = o; }
.LBB0_721:
	s_waitcnt lgkmcnt(2)
	v_mov_b32_e32 v23, v18
	v_mov_b32_e32 v18, v5
	v_mov_b32_e32 v22, v4
	v_pk_mul_f32 v[4:5], v[10:11], v[18:19]
	s_waitcnt lgkmcnt(0)
	v_mov_b32_e32 v19, v16
	v_mov_b32_e32 v16, v15
	v_mov_b32_e32 v18, v14
	v_pk_mul_f32 v[14:15], v[6:7], v[16:17]
	v_pk_mul_f32 v[22:23], v[12:13], v[22:23]
	v_pk_mul_f32 v[18:19], v[8:9], v[18:19]
	v_cvt_pk_bf16_f32 v16, v18, v14
	v_cvt_pk_bf16_f32 v14, v22, v4
	v_add_u32_e32 v4, s23, v20
	v_cvt_pk_bf16_f32 v17, v19, v15
	v_cvt_pk_bf16_f32 v15, v23, v5
	v_ashrrev_i32_e32 v5, 31, v4
	v_mul_lo_u32 v18, s86, v5
	v_mul_lo_u32 v19, s87, v4
	v_mad_u64_u32 v[4:5], s[0:1], s86, v4, 0
	v_add3_u32 v5, v5, v18, v19
	v_lshl_add_u64 v[4:5], v[4:5], 1, s[88:89]
	v_lshl_add_u64 v[4:5], s[34:35], 1, v[4:5]
	v_lshl_add_u64 v[4:5], v[4:5], 0, v[2:3]
	global_store_dwordx4 v[4:5], v[14:17], off sc1
	ds_read2_b32 v[14:15], v135 offset0:24 offset1:57
	ds_read2_b32 v[16:17], v135 offset0:90 offset1:123
	ds_read2_b32 v[4:5], v135 offset0:156 offset1:189
	ds_read2_b32 v[18:19], v135 offset0:222 offset1:255
	v_add_u32_e32 v21, s14, v134
	s_cmp_gt_i32 s22, 1
	s_mov_b64 s[0:1], -1
	s_cbranch_scc0 .LBB0_727
	s_movk_i32 s0, 0xaff
	v_cmp_lt_i32_e32 vcc, s0, v21
	v_lshlrev_b32_e32 v23, 1, v21
	v_and_b32_e32 v22, 0x7f, v21
	s_and_saveexec_b64 s[0:1], vcc
	s_xor_b64 s[0:1], exec, s[0:1]
	v_add_u32_e32 v20, 0x7fffea00, v23
	v_and_b32_e32 v20, 0x7fffff00, v20
	s_movk_i32 s4, 0x80
	v_or3_b32 v20, v22, v20, s4
	s_andn2_saveexec_b64 s[0:1], s[0:1]
	s_movk_i32 s4, 0xff00
	v_and_or_b32 v20, v23, s4, v22
	s_or_b64 exec, exec, s[0:1]
	s_mov_b64 s[0:1], 0

; #define GAS __attribute__((address_space(1)))
; #define LAS __attribute__((address_space(3)))
; #define LDS_WAIT() asm volatile("s_waitcnt lgkmcnt(0)" ::: "memory")
; __device__ __forceinline__ unsigned pk2(float lo, float hi) { return f2bf(lo) | (f2bf(hi) << 16); }
; template <bool WT> __device__ __forceinline__ void cvt_process(const CvtItem& ci, const CvtLoad& L, LAS float* scr, int lane) {
;     ...
;     for (int j = 0; j < 4; ++j) { const int n = (lane >> 3) + 8 * j; const LAS float* s = scr + (8 * c) * 33 + n;
;         v4u o; o.x = pk2(s[0 * 33] * g0.x, s[1 * 33] * g0.y); o.y = pk2(s[2 * 33] * g0.z, s[3 * 33] * g0.w); o.z = pk2(s[4 * 33] * g1.x, s[5 * 33] * g1.y); o.w = pk2(s[6 * 33] * g1.z, s[7 * 33] * g1.w);
;         GAS v4u* dp = (GAS v4u*)(ci.WT + (size_t)(ci.row_off + wrow_map(ci.mode, n0 + n)) * ci.K + k0 + 8 * c);
;         if constexpr (WT) asm volatile("global_store_dwordx4 %0, %1, off sc1" :: "v"(dp), "v"(o) : "memory"); else if (ci.late) __builtin_nontemporal_store(o, dp); else *dp = o; }
;     LDS_WAIT(); asm volatile("" ::: "memory");
.LBB0_1488:
	s_waitcnt lgkmcnt(3)
	v_mov_b32_e32 v22, v15
	s_waitcnt lgkmcnt(2)
	v_mov_b32_e32 v15, v16
	v_mov_b32_e32 v23, v17
	v_pk_mul_f32 v[12:13], v[12:13], v[14:15]
	s_waitcnt lgkmcnt(1)
	v_mov_b32_e32 v14, v5
	s_waitcnt lgkmcnt(0)
	v_mov_b32_e32 v15, v19
	v_pk_mul_f32 v[10:11], v[10:11], v[22:23]
	v_pk_mul_f32 v[6:7], v[6:7], v[14:15]
	v_mov_b32_e32 v5, v18
	v_pk_mul_f32 v[4:5], v[8:9], v[4:5]
	v_cvt_pk_bf16_f32 v6, v4, v6
	v_cvt_pk_bf16_f32 v4, v12, v10
	v_add_u32_e32 v8, s16, v20
	v_cvt_pk_bf16_f32 v7, v5, v7
	v_cvt_pk_bf16_f32 v5, v13, v11
	v_ashrrev_i32_e32 v9, 31, v8
	v_mul_lo_u32 v10, s84, v9
	v_mul_lo_u32 v11, s85, v8
	v_mad_u64_u32 v[8:9], s[0:1], s84, v8, 0
	v_add3_u32 v9, v9, v10, v11
	v_lshl_add_u64 v[8:9], v[8:9], 1, s[86:87]
	v_lshl_add_u64 v[8:9], s[34:35], 1, v[8:9]
	v_lshl_add_u64 v[8:9], v[8:9], 0, v[2:3]
	global_store_dwordx4 v[8:9], v[4:7], off sc1
	s_waitcnt lgkmcnt(0)

; #define GAS __attribute__((address_space(1)))
; #define LAS __attribute__((address_space(3)))
; #define LDS_WAIT() asm volatile("s_waitcnt lgkmcnt(0)" ::: "memory")
; __device__ __forceinline__ unsigned pk2(float lo, float hi) { return f2bf(lo) | (f2bf(hi) << 16); }
; __device__ __forceinline__ int wrow_map(int mode, int n) {
;     if (mode == 1) { if (n >= 1024 && n < 2048) { const int d = n & 63; return (n & ~63) + 32 * ((d >> 4) & 1) + 8 * ((d >> 2) & 3) + 4 * (d >> 5) + (d & 3); } return n; }
;     if (mode == 2) { if (n < DFF) return 256 * (n >> 7) + (n & 127); const int n2 = n - DFF; return 256 * (n2 >> 7) + 128 + (n2 & 127); }
;     return n;
; template <bool WT> __device__ __forceinline__ void cvt_process(const CvtItem& ci, const CvtLoad& L, LAS float* scr, int lane) {
;     ...
;     const int c = lane & 7; const bool hg = ci.gk != nullptr;
;     f32x4 g0, g1;
; #pragma unroll
;     for (int e = 0; e < 4; ++e) { g0[e] = hg ? L.g0[e] : 1.f; g1[e] = hg ? L.g1[e] : 1.f; }
;     LDS_WAIT(); asm volatile("" ::: "memory");
; #pragma unroll
;     for (int j = 0; j < 4; ++j) { const int n = (lane >> 3) + 8 * j; const LAS float* s = scr + (8 * c) * 33 + n;
;         v4u o; o.x = pk2(s[0 * 33] * g0.x, s[1 * 33] * g0.y); o.y = pk2(s[2 * 33] * g0.z, s[3 * 33] * g0.w); o.z = pk2(s[4 * 33] * g1.x, s[5 * 33] * g1.y); o.w = pk2(s[6 * 33] * g1.z, s[7 * 33] * g1.w);
;         GAS v4u* dp = (GAS v4u*)(ci.WT + (size_t)(ci.row_off + wrow_map(ci.mode, n0 + n)) * ci.K + k0 + 8 * c);
;         if constexpr (WT) asm volatile("global_store_dwordx4 %0, %1, off sc1" :: "v"(dp), "v"(o) : "memory"); else if (ci.late) __builtin_nontemporal_store(o, dp); else *dp = o; }
.LBB0_1552:
	v_cndmask_b32_e64 v93, v90, 1.0, s[8:9]
	v_cndmask_b32_e64 v91, v91, 1.0, s[8:9]
	v_cndmask_b32_e64 v90, v89, 1.0, s[8:9]
	v_cndmask_b32_e64 v89, v86, 1.0, s[8:9]
	v_cndmask_b32_e64 v86, v85, 1.0, s[8:9]
	s_waitcnt lgkmcnt(2)
	v_mov_b32_e32 v85, v100
	v_mov_b32_e32 v100, v95
	v_cndmask_b32_e64 v92, v88, 1.0, s[8:9]
	v_cndmask_b32_e64 v88, v84, 1.0, s[8:9]
	v_cndmask_b32_e64 v87, v87, 1.0, s[8:9]
	v_mov_b32_e32 v84, v94
	v_pk_mul_f32 v[94:95], v[90:91], v[100:101]
	s_waitcnt lgkmcnt(0)
	v_mov_b32_e32 v101, v98
	v_mov_b32_e32 v98, v97
	v_mov_b32_e32 v100, v96
	v_pk_mul_f32 v[96:97], v[86:87], v[98:99]
	v_pk_mul_f32 v[84:85], v[92:93], v[84:85]
	v_pk_mul_f32 v[100:101], v[88:89], v[100:101]
	v_add_u32_e32 v2, s19, v2
	v_cvt_pk_bf16_f32 v94, v84, v94
	v_ashrrev_i32_e32 v84, 31, v2
	v_cvt_pk_bf16_f32 v97, v101, v97
	v_cvt_pk_bf16_f32 v96, v100, v96
	v_cvt_pk_bf16_f32 v95, v85, v95
	v_mul_lo_u32 v98, s94, v84
	v_mul_lo_u32 v99, s95, v2
	v_mad_u64_u32 v[84:85], s[8:9], s94, v2, 0
	v_add3_u32 v85, v85, v98, v99
	v_lshl_add_u64 v[84:85], v[84:85], 1, s[92:93]
	v_lshl_add_u64 v[84:85], s[30:31], 1, v[84:85]
	v_lshlrev_b32_e32 v2, 1, v124
	v_lshl_add_u64 v[84:85], v[84:85], 0, v[2:3]
	global_store_dwordx4 v[84:85], v[94:97], off sc1
	ds_read2_b32 v[84:85], v135 offset0:8 offset1:41
	ds_read2_b32 v[98:99], v135 offset0:74 offset1:107
	ds_read2_b32 v[94:95], v135 offset0:140 offset1:173
	ds_read2_b32 v[96:97], v135 offset0:206 offset1:239
	v_add_u32_e32 v101, s0, v132
	s_cmp_gt_i32 s38, 1
	s_mov_b64 s[8:9], -1
	s_cbranch_scc0 .LBB0_1558
	s_movk_i32 s1, 0xaff
	v_cmp_lt_i32_e32 vcc, s1, v101
	v_lshlrev_b32_e32 v114, 1, v101
	v_and_b32_e32 v113, 0x7f, v101
	s_and_saveexec_b64 s[8:9], vcc
	s_xor_b64 s[8:9], exec, s[8:9]
	v_add_u32_e32 v100, 0x7fffea00, v114
	v_and_b32_e32 v100, 0x7fffff00, v100
	s_movk_i32 s1, 0x80
	v_or3_b32 v100, v113, v100, s1
	s_andn2_saveexec_b64 s[8:9], s[8:9]
	s_movk_i32 s1, 0xff00
	v_and_or_b32 v100, v114, s1, v113
	s_or_b64 exec, exec, s[8:9]
	s_mov_b64 s[8:9], 0

; #define GAS __attribute__((address_space(1)))
; #define LAS __attribute__((address_space(3)))
; __device__ __forceinline__ unsigned pk2(float lo, float hi) { return f2bf(lo) | (f2bf(hi) << 16); }
; __device__ __forceinline__ int wrow_map(int mode, int n) {
;     if (mode == 1) { if (n >= 1024 && n < 2048) { const int d = n & 63; return (n & ~63) + 32 * ((d >> 4) & 1) + 8 * ((d >> 2) & 3) + 4 * (d >> 5) + (d & 3); } return n; }
;     if (mode == 2) { if (n < DFF) return 256 * (n >> 7) + (n & 127); const int n2 = n - DFF; return 256 * (n2 >> 7) + 128 + (n2 & 127); }
;     return n;
; template <bool WT> __device__ __forceinline__ void cvt_process(const CvtItem& ci, const CvtLoad& L, LAS float* scr, int lane) {
;     ...
;     for (int j = 0; j < 4; ++j) { const int n = (lane >> 3) + 8 * j; const LAS float* s = scr + (8 * c) * 33 + n;
;         v4u o; o.x = pk2(s[0 * 33] * g0.x, s[1 * 33] * g0.y); o.y = pk2(s[2 * 33] * g0.z, s[3 * 33] * g0.w); o.z = pk2(s[4 * 33] * g1.x, s[5 * 33] * g1.y); o.w = pk2(s[6 * 33] * g1.z, s[7 * 33] * g1.w);
;         GAS v4u* dp = (GAS v4u*)(ci.WT + (size_t)(ci.row_off + wrow_map(ci.mode, n0 + n)) * ci.K + k0 + 8 * c);
;         if constexpr (WT) asm volatile("global_store_dwordx4 %0, %1, off sc1" :: "v"(dp), "v"(o) : "memory"); else if (ci.late) __builtin_nontemporal_store(o, dp); else *dp = o; }
.LBB0_1562:
	s_waitcnt lgkmcnt(2)
	v_mov_b32_e32 v115, v98
	v_mov_b32_e32 v98, v85
	v_mov_b32_e32 v114, v84
	v_pk_mul_f32 v[84:85], v[90:91], v[98:99]
	s_waitcnt lgkmcnt(0)
	v_mov_b32_e32 v99, v96
	v_mov_b32_e32 v96, v95
	v_mov_b32_e32 v98, v94
	v_pk_mul_f32 v[94:95], v[86:87], v[96:97]
	v_pk_mul_f32 v[114:115], v[92:93], v[114:115]
	v_pk_mul_f32 v[98:99], v[88:89], v[98:99]
	v_cvt_pk_bf16_f32 v96, v98, v94
	v_cvt_pk_bf16_f32 v94, v114, v84
	v_add_u32_e32 v84, s19, v100
	v_cvt_pk_bf16_f32 v97, v99, v95
	v_cvt_pk_bf16_f32 v95, v115, v85
	v_ashrrev_i32_e32 v85, 31, v84
	v_mul_lo_u32 v98, s94, v85
	v_mul_lo_u32 v99, s95, v84
	v_mad_u64_u32 v[84:85], s[8:9], s94, v84, 0
	v_add3_u32 v85, v85, v98, v99
	v_lshl_add_u64 v[84:85], v[84:85], 1, s[92:93]
	v_lshl_add_u64 v[84:85], s[30:31], 1, v[84:85]
	v_lshl_add_u64 v[84:85], v[84:85], 0, v[2:3]
	global_store_dwordx4 v[84:85], v[94:97], off sc1
	ds_read2_b32 v[84:85], v135 offset0:16 offset1:49
	ds_read2_b32 v[98:99], v135 offset0:82 offset1:115
	ds_read2_b32 v[94:95], v135 offset0:148 offset1:181
	ds_read2_b32 v[96:97], v135 offset0:214 offset1:247
	v_add_u32_e32 v101, s0, v133
	s_cmp_gt_i32 s38, 1
	s_mov_b64 s[8:9], -1
	s_cbranch_scc0 .LBB0_1568
	s_movk_i32 s1, 0xaff
	v_cmp_lt_i32_e32 vcc, s1, v101
	v_lshlrev_b32_e32 v114, 1, v101
	v_and_b32_e32 v113, 0x7f, v101
	s_and_saveexec_b64 s[8:9], vcc
	s_xor_b64 s[8:9], exec, s[8:9]
	v_add_u32_e32 v100, 0x7fffea00, v114
	v_and_b32_e32 v100, 0x7fffff00, v100
	s_movk_i32 s1, 0x80
	v_or3_b32 v100, v113, v100, s1
	s_andn2_saveexec_b64 s[8:9], s[8:9]
	s_movk_i32 s1, 0xff00
	v_and_or_b32 v100, v114, s1, v113
	s_or_b64 exec, exec, s[8:9]
	s_mov_b64 s[8:9], 0

; #define GAS __attribute__((address_space(1)))
; #define LAS __attribute__((address_space(3)))
; __device__ __forceinline__ unsigned pk2(float lo, float hi) { return f2bf(lo) | (f2bf(hi) << 16); }
; __device__ __forceinline__ int wrow_map(int mode, int n) {
;     if (mode == 1) { if (n >= 1024 && n < 2048) { const int d = n & 63; return (n & ~63) + 32 * ((d >> 4) & 1) + 8 * ((d >> 2) & 3) + 4 * (d >> 5) + (d & 3); } return n; }
;     if (mode == 2) { if (n < DFF) return 256 * (n >> 7) + (n & 127); const int n2 = n - DFF; return 256 * (n2 >> 7) + 128 + (n2 & 127); }
;     return n;
; template <bool WT> __device__ __forceinline__ void cvt_process(const CvtItem& ci, const CvtLoad& L, LAS float* scr, int lane) {
;     ...
;     for (int j = 0; j < 4; ++j) { const int n = (lane >> 3) + 8 * j; const LAS float* s = scr + (8 * c) * 33 + n;
;         v4u o; o.x = pk2(s[0 * 33] * g0.x, s[1 * 33] * g0.y); o.y = pk2(s[2 * 33] * g0.z, s[3 * 33] * g0.w); o.z = pk2(s[4 * 33] * g1.x, s[5 * 33] * g1.y); o.w = pk2(s[6 * 33] * g1.z, s[7 * 33] * g1.w);
;         GAS v4u* dp = (GAS v4u*)(ci.WT + (size_t)(ci.row_off + wrow_map(ci.mode, n0 + n)) * ci.K + k0 + 8 * c);
;         if constexpr (WT) asm volatile("global_store_dwordx4 %0, %1, off sc1" :: "v"(dp), "v"(o) : "memory"); else if (ci.late) __builtin_nontemporal_store(o, dp); else *dp = o; }
.LBB0_1572:
	s_waitcnt lgkmcnt(2)
	v_mov_b32_e32 v115, v98
	v_mov_b32_e32 v98, v85
	v_mov_b32_e32 v114, v84
	v_pk_mul_f32 v[84:85], v[90:91], v[98:99]
	s_waitcnt lgkmcnt(0)
	v_mov_b32_e32 v99, v96
	v_mov_b32_e32 v96, v95
	v_mov_b32_e32 v98, v94
	v_pk_mul_f32 v[94:95], v[86:87], v[96:97]
	v_pk_mul_f32 v[114:115], v[92:93], v[114:115]
	v_pk_mul_f32 v[98:99], v[88:89], v[98:99]
	v_cvt_pk_bf16_f32 v96, v98, v94
	v_cvt_pk_bf16_f32 v94, v114, v84
	v_add_u32_e32 v84, s19, v100
	v_cvt_pk_bf16_f32 v97, v99, v95
	v_cvt_pk_bf16_f32 v95, v115, v85
	v_ashrrev_i32_e32 v85, 31, v84
	v_mul_lo_u32 v98, s94, v85
	v_mul_lo_u32 v99, s95, v84
	v_mad_u64_u32 v[84:85], s[8:9], s94, v84, 0
	v_add3_u32 v85, v85, v98, v99
	v_lshl_add_u64 v[84:85], v[84:85], 1, s[92:93]
	v_lshl_add_u64 v[84:85], s[30:31], 1, v[84:85]
	v_lshl_add_u64 v[84:85], v[84:85], 0, v[2:3]
	global_store_dwordx4 v[84:85], v[94:97], off sc1
	ds_read2_b32 v[94:95], v135 offset0:24 offset1:57
	ds_read2_b32 v[96:97], v135 offset0:90 offset1:123
	ds_read2_b32 v[84:85], v135 offset0:156 offset1:189
	ds_read2_b32 v[100:101], v135 offset0:222 offset1:255
	s_cmp_gt_i32 s38, 1
	s_waitcnt lgkmcnt(3)
	v_mov_b32_e32 v98, v95
	s_waitcnt lgkmcnt(2)
	v_mov_b32_e32 v95, v96
	v_mov_b32_e32 v99, v97
	s_waitcnt lgkmcnt(1)
	v_mov_b32_e32 v96, v85
	s_waitcnt lgkmcnt(0)
	v_mov_b32_e32 v85, v100
	v_mov_b32_e32 v97, v101
	v_add_u32_e32 v101, s0, v134
	s_mov_b64 s[0:1], -1
	s_cbranch_scc0 .LBB0_1578
	s_movk_i32 s0, 0xaff
	v_cmp_lt_i32_e32 vcc, s0, v101
	v_lshlrev_b32_e32 v114, 1, v101
	v_and_b32_e32 v113, 0x7f, v101
	s_and_saveexec_b64 s[0:1], vcc
	s_xor_b64 s[0:1], exec, s[0:1]
	v_add_u32_e32 v100, 0x7fffea00, v114
	v_and_b32_e32 v100, 0x7fffff00, v100
	s_movk_i32 s8, 0x80
	v_or3_b32 v100, v113, v100, s8
	s_andn2_saveexec_b64 s[0:1], s[0:1]
	s_movk_i32 s8, 0xff00
	v_and_or_b32 v100, v114, s8, v113
	s_or_b64 exec, exec, s[0:1]
	s_mov_b64 s[0:1], 0

; #define GAS __attribute__((address_space(1)))
; #define LAS __attribute__((address_space(3)))
; #define LDS_WAIT() asm volatile("s_waitcnt lgkmcnt(0)" ::: "memory")
; __device__ __forceinline__ unsigned pk2(float lo, float hi) { return f2bf(lo) | (f2bf(hi) << 16); }
; template <bool WT> __device__ __forceinline__ void cvt_process(const CvtItem& ci, const CvtLoad& L, LAS float* scr, int lane) {
;     ...
;     for (int j = 0; j < 4; ++j) { const int n = (lane >> 3) + 8 * j; const LAS float* s = scr + (8 * c) * 33 + n;
;         v4u o; o.x = pk2(s[0 * 33] * g0.x, s[1 * 33] * g0.y); o.y = pk2(s[2 * 33] * g0.z, s[3 * 33] * g0.w); o.z = pk2(s[4 * 33] * g1.x, s[5 * 33] * g1.y); o.w = pk2(s[6 * 33] * g1.z, s[7 * 33] * g1.w);
;         GAS v4u* dp = (GAS v4u*)(ci.WT + (size_t)(ci.row_off + wrow_map(ci.mode, n0 + n)) * ci.K + k0 + 8 * c);
;         if constexpr (WT) asm volatile("global_store_dwordx4 %0, %1, off sc1" :: "v"(dp), "v"(o) : "memory"); else if (ci.late) __builtin_nontemporal_store(o, dp); else *dp = o; }
;     LDS_WAIT(); asm volatile("" ::: "memory");
.LBB0_1582:
	v_pk_mul_f32 v[90:91], v[90:91], v[98:99]
	v_pk_mul_f32 v[86:87], v[86:87], v[96:97]
	v_pk_mul_f32 v[92:93], v[92:93], v[94:95]
	v_pk_mul_f32 v[84:85], v[88:89], v[84:85]
	v_cvt_pk_bf16_f32 v86, v84, v86
	v_cvt_pk_bf16_f32 v84, v92, v90
	v_add_u32_e32 v88, s19, v100
	v_cvt_pk_bf16_f32 v87, v85, v87
	v_cvt_pk_bf16_f32 v85, v93, v91
	v_ashrrev_i32_e32 v89, 31, v88
	v_mul_lo_u32 v90, s94, v89
	v_mul_lo_u32 v91, s95, v88
	v_mad_u64_u32 v[88:89], s[0:1], s94, v88, 0
	v_add3_u32 v89, v89, v90, v91
	v_lshl_add_u64 v[88:89], v[88:89], 1, s[92:93]
	v_lshl_add_u64 v[88:89], s[30:31], 1, v[88:89]
	v_lshl_add_u64 v[88:89], v[88:89], 0, v[2:3]
	global_store_dwordx4 v[88:89], v[84:87], off sc1
	s_waitcnt lgkmcnt(0)
	s_andn2_b64 vcc, exec, s[26:27]
	s_cbranch_vccz .LBB0_1584
	s_andn2_b64 vcc, exec, s[20:21]
	s_cbranch_vccnz .LBB0_1489
	s_branch .LBB0_1625

; #define GAS __attribute__((address_space(1)))
; #define LAS __attribute__((address_space(3)))
; #define LDS_WAIT() asm volatile("s_waitcnt lgkmcnt(0)" ::: "memory")
; __device__ __forceinline__ unsigned pk2(float lo, float hi) { return f2bf(lo) | (f2bf(hi) << 16); }
; __device__ __forceinline__ int wrow_map(int mode, int n) {
;     if (mode == 1) { if (n >= 1024 && n < 2048) { const int d = n & 63; return (n & ~63) + 32 * ((d >> 4) & 1) + 8 * ((d >> 2) & 3) + 4 * (d >> 5) + (d & 3); } return n; }
;     if (mode == 2) { if (n < DFF) return 256 * (n >> 7) + (n & 127); const int n2 = n - DFF; return 256 * (n2 >> 7) + 128 + (n2 & 127); }
;     return n;
; template <bool WT> __device__ __forceinline__ void cvt_process(const CvtItem& ci, const CvtLoad& L, LAS float* scr, int lane) {
;     ...
;     const int c = lane & 7; const bool hg = ci.gk != nullptr;
;     f32x4 g0, g1;
; #pragma unroll
;     for (int e = 0; e < 4; ++e) { g0[e] = hg ? L.g0[e] : 1.f; g1[e] = hg ? L.g1[e] : 1.f; }
;     LDS_WAIT(); asm volatile("" ::: "memory");
; #pragma unroll
;     for (int j = 0; j < 4; ++j) { const int n = (lane >> 3) + 8 * j; const LAS float* s = scr + (8 * c) * 33 + n;
;         v4u o; o.x = pk2(s[0 * 33] * g0.x, s[1 * 33] * g0.y); o.y = pk2(s[2 * 33] * g0.z, s[3 * 33] * g0.w); o.z = pk2(s[4 * 33] * g1.x, s[5 * 33] * g1.y); o.w = pk2(s[6 * 33] * g1.z, s[7 * 33] * g1.w);
;         GAS v4u* dp = (GAS v4u*)(ci.WT + (size_t)(ci.row_off + wrow_map(ci.mode, n0 + n)) * ci.K + k0 + 8 * c);
;         if constexpr (WT) asm volatile("global_store_dwordx4 %0, %1, off sc1" :: "v"(dp), "v"(o) : "memory"); else if (ci.late) __builtin_nontemporal_store(o, dp); else *dp = o; }
.LBB0_1594:
	v_cndmask_b32_e64 v53, v50, 1.0, s[6:7]
	v_cndmask_b32_e64 v51, v51, 1.0, s[6:7]
	v_cndmask_b32_e64 v50, v49, 1.0, s[6:7]
	v_cndmask_b32_e64 v49, v46, 1.0, s[6:7]
	v_cndmask_b32_e64 v46, v45, 1.0, s[6:7]
	s_waitcnt lgkmcnt(2)
	v_mov_b32_e32 v45, v60
	v_mov_b32_e32 v60, v55
	v_cndmask_b32_e64 v52, v48, 1.0, s[6:7]
	v_cndmask_b32_e64 v48, v44, 1.0, s[6:7]
	v_cndmask_b32_e64 v47, v47, 1.0, s[6:7]
	v_mov_b32_e32 v44, v54
	v_pk_mul_f32 v[54:55], v[50:51], v[60:61]
	s_waitcnt lgkmcnt(0)
	v_mov_b32_e32 v61, v58
	v_mov_b32_e32 v58, v57
	v_mov_b32_e32 v60, v56
	v_pk_mul_f32 v[56:57], v[46:47], v[58:59]
	v_pk_mul_f32 v[44:45], v[52:53], v[44:45]
	v_pk_mul_f32 v[60:61], v[48:49], v[60:61]
	v_cvt_pk_bf16_f32 v54, v44, v54
	v_add_u32_e32 v44, s18, v62
	v_cvt_pk_bf16_f32 v55, v45, v55
	v_ashrrev_i32_e32 v45, 31, v44
	v_cvt_pk_bf16_f32 v57, v61, v57
	v_cvt_pk_bf16_f32 v56, v60, v56
	v_mul_lo_u32 v58, s88, v45
	v_mul_lo_u32 v59, s89, v44
	v_mad_u64_u32 v[44:45], s[0:1], s88, v44, 0
	v_add3_u32 v45, v45, v58, v59
	v_lshl_add_u64 v[44:45], v[44:45], 1, s[90:91]
	v_lshl_add_u64 v[44:45], s[40:41], 1, v[44:45]
	v_lshl_add_u64 v[44:45], v[44:45], 0, v[2:3]
	global_store_dwordx4 v[44:45], v[54:57], off sc1
	ds_read2_b32 v[44:45], v135 offset0:8 offset1:41
	ds_read2_b32 v[58:59], v135 offset0:74 offset1:107
	ds_read2_b32 v[54:55], v135 offset0:140 offset1:173
	ds_read2_b32 v[56:57], v135 offset0:206 offset1:239
	v_add_u32_e32 v61, s28, v132
	s_cmp_gt_i32 s17, 1
	s_mov_b64 s[0:1], -1
	s_cbranch_scc0 .LBB0_1600
	s_movk_i32 s0, 0xaff
	v_cmp_lt_i32_e32 vcc, s0, v61
	v_lshlrev_b32_e32 v63, 1, v61
	v_and_b32_e32 v62, 0x7f, v61
	s_and_saveexec_b64 s[0:1], vcc
	s_xor_b64 s[0:1], exec, s[0:1]
	v_add_u32_e32 v60, 0x7fffea00, v63
	v_and_b32_e32 v60, 0x7fffff00, v60
	s_movk_i32 s6, 0x80
	v_or3_b32 v60, v62, v60, s6
	s_andn2_saveexec_b64 s[0:1], s[0:1]
	s_movk_i32 s6, 0xff00
	v_and_or_b32 v60, v63, s6, v62
	s_or_b64 exec, exec, s[0:1]
	s_mov_b64 s[0:1], 0

; #define GAS __attribute__((address_space(1)))
; #define LAS __attribute__((address_space(3)))
; __device__ __forceinline__ unsigned pk2(float lo, float hi) { return f2bf(lo) | (f2bf(hi) << 16); }
; __device__ __forceinline__ int wrow_map(int mode, int n) {
;     if (mode == 1) { if (n >= 1024 && n < 2048) { const int d = n & 63; return (n & ~63) + 32 * ((d >> 4) & 1) + 8 * ((d >> 2) & 3) + 4 * (d >> 5) + (d & 3); } return n; }
;     if (mode == 2) { if (n < DFF) return 256 * (n >> 7) + (n & 127); const int n2 = n - DFF; return 256 * (n2 >> 7) + 128 + (n2 & 127); }
;     return n;
; template <bool WT> __device__ __forceinline__ void cvt_process(const CvtItem& ci, const CvtLoad& L, LAS float* scr, int lane) {
;     ...
;     for (int j = 0; j < 4; ++j) { const int n = (lane >> 3) + 8 * j; const LAS float* s = scr + (8 * c) * 33 + n;
;         v4u o; o.x = pk2(s[0 * 33] * g0.x, s[1 * 33] * g0.y); o.y = pk2(s[2 * 33] * g0.z, s[3 * 33] * g0.w); o.z = pk2(s[4 * 33] * g1.x, s[5 * 33] * g1.y); o.w = pk2(s[6 * 33] * g1.z, s[7 * 33] * g1.w);
;         GAS v4u* dp = (GAS v4u*)(ci.WT + (size_t)(ci.row_off + wrow_map(ci.mode, n0 + n)) * ci.K + k0 + 8 * c);
;         if constexpr (WT) asm volatile("global_store_dwordx4 %0, %1, off sc1" :: "v"(dp), "v"(o) : "memory"); else if (ci.late) __builtin_nontemporal_store(o, dp); else *dp = o; }
.LBB0_1604:
	s_waitcnt lgkmcnt(2)
	v_mov_b32_e32 v63, v58
	v_mov_b32_e32 v58, v45
	v_mov_b32_e32 v62, v44
	v_pk_mul_f32 v[44:45], v[50:51], v[58:59]
	s_waitcnt lgkmcnt(0)
	v_mov_b32_e32 v59, v56
	v_mov_b32_e32 v56, v55
	v_mov_b32_e32 v58, v54
	v_pk_mul_f32 v[54:55], v[46:47], v[56:57]
	v_pk_mul_f32 v[62:63], v[52:53], v[62:63]
	v_pk_mul_f32 v[58:59], v[48:49], v[58:59]
	v_cvt_pk_bf16_f32 v56, v58, v54
	v_cvt_pk_bf16_f32 v54, v62, v44
	v_add_u32_e32 v44, s18, v60
	v_cvt_pk_bf16_f32 v57, v59, v55
	v_cvt_pk_bf16_f32 v55, v63, v45
	v_ashrrev_i32_e32 v45, 31, v44
	v_mul_lo_u32 v58, s88, v45
	v_mul_lo_u32 v59, s89, v44
	v_mad_u64_u32 v[44:45], s[0:1], s88, v44, 0
	v_add3_u32 v45, v45, v58, v59
	v_lshl_add_u64 v[44:45], v[44:45], 1, s[90:91]
	v_lshl_add_u64 v[44:45], s[40:41], 1, v[44:45]
	v_lshl_add_u64 v[44:45], v[44:45], 0, v[2:3]
	global_store_dwordx4 v[44:45], v[54:57], off sc1
	ds_read2_b32 v[44:45], v135 offset0:16 offset1:49
	ds_read2_b32 v[58:59], v135 offset0:82 offset1:115
	ds_read2_b32 v[54:55], v135 offset0:148 offset1:181
	ds_read2_b32 v[56:57], v135 offset0:214 offset1:247
	v_add_u32_e32 v61, s28, v133
	s_cmp_gt_i32 s17, 1
	s_mov_b64 s[0:1], -1
	s_cbranch_scc0 .LBB0_1610
	s_movk_i32 s0, 0xaff
	v_cmp_lt_i32_e32 vcc, s0, v61
	v_lshlrev_b32_e32 v63, 1, v61
	v_and_b32_e32 v62, 0x7f, v61
	s_and_saveexec_b64 s[0:1], vcc
	s_xor_b64 s[0:1], exec, s[0:1]
	v_add_u32_e32 v60, 0x7fffea00, v63
	v_and_b32_e32 v60, 0x7fffff00, v60
	s_movk_i32 s6, 0x80
	v_or3_b32 v60, v62, v60, s6
	s_andn2_saveexec_b64 s[0:1], s[0:1]
	s_movk_i32 s6, 0xff00
	v_and_or_b32 v60, v63, s6, v62
	s_or_b64 exec, exec, s[0:1]
	s_mov_b64 s[0:1], 0

; #define GAS __attribute__((address_space(1)))
; #define LAS __attribute__((address_space(3)))
; __device__ __forceinline__ unsigned pk2(float lo, float hi) { return f2bf(lo) | (f2bf(hi) << 16); }
; __device__ __forceinline__ int wrow_map(int mode, int n) {
;     if (mode == 1) { if (n >= 1024 && n < 2048) { const int d = n & 63; return (n & ~63) + 32 * ((d >> 4) & 1) + 8 * ((d >> 2) & 3) + 4 * (d >> 5) + (d & 3); } return n; }
;     if (mode == 2) { if (n < DFF) return 256 * (n >> 7) + (n & 127); const int n2 = n - DFF; return 256 * (n2 >> 7) + 128 + (n2 & 127); }
;     return n;
; template <bool WT> __device__ __forceinline__ void cvt_process(const CvtItem& ci, const CvtLoad& L, LAS float* scr, int lane) {
;     ...
;     for (int j = 0; j < 4; ++j) { const int n = (lane >> 3) + 8 * j; const LAS float* s = scr + (8 * c) * 33 + n;
;         v4u o; o.x = pk2(s[0 * 33] * g0.x, s[1 * 33] * g0.y); o.y = pk2(s[2 * 33] * g0.z, s[3 * 33] * g0.w); o.z = pk2(s[4 * 33] * g1.x, s[5 * 33] * g1.y); o.w = pk2(s[6 * 33] * g1.z, s[7 * 33] * g1.w);
;         GAS v4u* dp = (GAS v4u*)(ci.WT + (size_t)(ci.row_off + wrow_map(ci.mode, n0 + n)) * ci.K + k0 + 8 * c);
;         if constexpr (WT) asm volatile("global_store_dwordx4 %0, %1, off sc1" :: "v"(dp), "v"(o) : "memory"); else if (ci.late) __builtin_nontemporal_store(o, dp); else *dp = o; }
.LBB0_1614:
	s_waitcnt lgkmcnt(2)
	v_mov_b32_e32 v63, v58
	v_mov_b32_e32 v58, v45
	v_mov_b32_e32 v62, v44
	v_pk_mul_f32 v[44:45], v[50:51], v[58:59]
	s_waitcnt lgkmcnt(0)
	v_mov_b32_e32 v59, v56
	v_mov_b32_e32 v56, v55
	v_mov_b32_e32 v58, v54
	v_pk_mul_f32 v[54:55], v[46:47], v[56:57]
	v_pk_mul_f32 v[62:63], v[52:53], v[62:63]
	v_pk_mul_f32 v[58:59], v[48:49], v[58:59]
	v_cvt_pk_bf16_f32 v56, v58, v54
	v_cvt_pk_bf16_f32 v54, v62, v44
	v_add_u32_e32 v44, s18, v60
	v_cvt_pk_bf16_f32 v57, v59, v55
	v_cvt_pk_bf16_f32 v55, v63, v45
	v_ashrrev_i32_e32 v45, 31, v44
	v_mul_lo_u32 v58, s88, v45
	v_mul_lo_u32 v59, s89, v44
	v_mad_u64_u32 v[44:45], s[0:1], s88, v44, 0
	v_add3_u32 v45, v45, v58, v59
	v_lshl_add_u64 v[44:45], v[44:45], 1, s[90:91]
	v_lshl_add_u64 v[44:45], s[40:41], 1, v[44:45]
	v_lshl_add_u64 v[44:45], v[44:45], 0, v[2:3]
	global_store_dwordx4 v[44:45], v[54:57], off sc1
	ds_read2_b32 v[54:55], v135 offset0:24 offset1:57
	ds_read2_b32 v[56:57], v135 offset0:90 offset1:123
	ds_read2_b32 v[44:45], v135 offset0:156 offset1:189
	ds_read2_b32 v[58:59], v135 offset0:222 offset1:255
	v_add_u32_e32 v61, s28, v134
	s_cmp_gt_i32 s17, 1
	s_mov_b64 s[0:1], -1
	s_cbranch_scc0 .LBB0_1620
	s_movk_i32 s0, 0xaff
	v_cmp_lt_i32_e32 vcc, s0, v61
	v_lshlrev_b32_e32 v63, 1, v61
	v_and_b32_e32 v62, 0x7f, v61
	s_and_saveexec_b64 s[0:1], vcc
	s_xor_b64 s[0:1], exec, s[0:1]
	v_add_u32_e32 v60, 0x7fffea00, v63
	v_and_b32_e32 v60, 0x7fffff00, v60
	s_movk_i32 s6, 0x80
	v_or3_b32 v60, v62, v60, s6
	s_andn2_saveexec_b64 s[0:1], s[0:1]
	s_movk_i32 s6, 0xff00
	v_and_or_b32 v60, v63, s6, v62
	s_or_b64 exec, exec, s[0:1]
	s_mov_b64 s[0:1], 0

; #define GAS __attribute__((address_space(1)))
; #define LAS __attribute__((address_space(3)))
; #define LDS_WAIT() asm volatile("s_waitcnt lgkmcnt(0)" ::: "memory")
; __device__ __forceinline__ unsigned pk2(float lo, float hi) { return f2bf(lo) | (f2bf(hi) << 16); }
; template <bool WT> __device__ __forceinline__ void cvt_process(const CvtItem& ci, const CvtLoad& L, LAS float* scr, int lane) {
;     ...
;     for (int j = 0; j < 4; ++j) { const int n = (lane >> 3) + 8 * j; const LAS float* s = scr + (8 * c) * 33 + n;
;         v4u o; o.x = pk2(s[0 * 33] * g0.x, s[1 * 33] * g0.y); o.y = pk2(s[2 * 33] * g0.z, s[3 * 33] * g0.w); o.z = pk2(s[4 * 33] * g1.x, s[5 * 33] * g1.y); o.w = pk2(s[6 * 33] * g1.z, s[7 * 33] * g1.w);
;         GAS v4u* dp = (GAS v4u*)(ci.WT + (size_t)(ci.row_off + wrow_map(ci.mode, n0 + n)) * ci.K + k0 + 8 * c);
;         if constexpr (WT) asm volatile("global_store_dwordx4 %0, %1, off sc1" :: "v"(dp), "v"(o) : "memory"); else if (ci.late) __builtin_nontemporal_store(o, dp); else *dp = o; }
;     LDS_WAIT(); asm volatile("" ::: "memory");
.LBB0_1624:
	s_waitcnt lgkmcnt(3)
	v_mov_b32_e32 v62, v55
	s_waitcnt lgkmcnt(2)
	v_mov_b32_e32 v55, v56
	v_mov_b32_e32 v63, v57
	v_pk_mul_f32 v[52:53], v[52:53], v[54:55]
	s_waitcnt lgkmcnt(1)
	v_mov_b32_e32 v54, v45
	s_waitcnt lgkmcnt(0)
	v_mov_b32_e32 v55, v59
	v_pk_mul_f32 v[50:51], v[50:51], v[62:63]
	v_pk_mul_f32 v[46:47], v[46:47], v[54:55]
	v_mov_b32_e32 v45, v58
	v_pk_mul_f32 v[44:45], v[48:49], v[44:45]
	v_cvt_pk_bf16_f32 v46, v44, v46
	v_cvt_pk_bf16_f32 v44, v52, v50
	v_add_u32_e32 v48, s18, v60
	v_cvt_pk_bf16_f32 v47, v45, v47
	v_cvt_pk_bf16_f32 v45, v53, v51
	v_ashrrev_i32_e32 v49, 31, v48
	v_mul_lo_u32 v50, s88, v49
	v_mul_lo_u32 v51, s89, v48
	v_mad_u64_u32 v[48:49], s[0:1], s88, v48, 0
	v_add3_u32 v49, v49, v50, v51
	v_lshl_add_u64 v[48:49], v[48:49], 1, s[90:91]
	v_lshl_add_u64 v[48:49], s[40:41], 1, v[48:49]
	v_lshl_add_u64 v[48:49], v[48:49], 0, v[2:3]
	global_store_dwordx4 v[48:49], v[44:47], off sc1
	s_waitcnt lgkmcnt(0)
	s_andn2_b64 vcc, exec, s[20:21]
	s_cbranch_vccnz .LBB0_1489

; #define GAS __attribute__((address_space(1)))
; #define LAS __attribute__((address_space(3)))
; #define LDS_WAIT() asm volatile("s_waitcnt lgkmcnt(0)" ::: "memory")
; __device__ __forceinline__ unsigned pk2(float lo, float hi) { return f2bf(lo) | (f2bf(hi) << 16); }
; __device__ __forceinline__ int wrow_map(int mode, int n) {
;     if (mode == 1) { if (n >= 1024 && n < 2048) { const int d = n & 63; return (n & ~63) + 32 * ((d >> 4) & 1) + 8 * ((d >> 2) & 3) + 4 * (d >> 5) + (d & 3); } return n; }
;     if (mode == 2) { if (n < DFF) return 256 * (n >> 7) + (n & 127); const int n2 = n - DFF; return 256 * (n2 >> 7) + 128 + (n2 & 127); }
;     return n;
; template <bool WT> __device__ __forceinline__ void cvt_process(const CvtItem& ci, const CvtLoad& L, LAS float* scr, int lane) {
;     ...
;     const int c = lane & 7; const bool hg = ci.gk != nullptr;
;     f32x4 g0, g1;
; #pragma unroll
;     for (int e = 0; e < 4; ++e) { g0[e] = hg ? L.g0[e] : 1.f; g1[e] = hg ? L.g1[e] : 1.f; }
;     LDS_WAIT(); asm volatile("" ::: "memory");
; #pragma unroll
;     for (int j = 0; j < 4; ++j) { const int n = (lane >> 3) + 8 * j; const LAS float* s = scr + (8 * c) * 33 + n;
;         v4u o; o.x = pk2(s[0 * 33] * g0.x, s[1 * 33] * g0.y); o.y = pk2(s[2 * 33] * g0.z, s[3 * 33] * g0.w); o.z = pk2(s[4 * 33] * g1.x, s[5 * 33] * g1.y); o.w = pk2(s[6 * 33] * g1.z, s[7 * 33] * g1.w);
;         GAS v4u* dp = (GAS v4u*)(ci.WT + (size_t)(ci.row_off + wrow_map(ci.mode, n0 + n)) * ci.K + k0 + 8 * c);
;         if constexpr (WT) asm volatile("global_store_dwordx4 %0, %1, off sc1" :: "v"(dp), "v"(o) : "memory"); else if (ci.late) __builtin_nontemporal_store(o, dp); else *dp = o; }
.LBB0_1635:
	v_cndmask_b32_e64 v13, v10, 1.0, s[4:5]
	v_cndmask_b32_e64 v11, v11, 1.0, s[4:5]
	v_cndmask_b32_e64 v10, v9, 1.0, s[4:5]
	v_cndmask_b32_e64 v9, v6, 1.0, s[4:5]
	v_cndmask_b32_e64 v6, v5, 1.0, s[4:5]
	s_waitcnt lgkmcnt(2)
	v_mov_b32_e32 v5, v20
	v_mov_b32_e32 v20, v15
	v_cndmask_b32_e64 v12, v8, 1.0, s[4:5]
	v_cndmask_b32_e64 v8, v4, 1.0, s[4:5]
	v_cndmask_b32_e64 v7, v7, 1.0, s[4:5]
	v_mov_b32_e32 v4, v14
	v_pk_mul_f32 v[14:15], v[10:11], v[20:21]
	s_waitcnt lgkmcnt(0)
	v_mov_b32_e32 v21, v18
	v_mov_b32_e32 v18, v17
	v_mov_b32_e32 v20, v16
	v_pk_mul_f32 v[16:17], v[6:7], v[18:19]
	v_pk_mul_f32 v[4:5], v[12:13], v[4:5]
	v_pk_mul_f32 v[20:21], v[8:9], v[20:21]
	v_cvt_pk_bf16_f32 v14, v4, v14
	v_add_u32_e32 v4, s16, v22
	v_cvt_pk_bf16_f32 v15, v5, v15
	v_ashrrev_i32_e32 v5, 31, v4
	v_cvt_pk_bf16_f32 v17, v21, v17
	v_cvt_pk_bf16_f32 v16, v20, v16
	v_mul_lo_u32 v18, s84, v5
	v_mul_lo_u32 v19, s85, v4
	v_mad_u64_u32 v[4:5], s[0:1], s84, v4, 0
	v_add3_u32 v5, v5, v18, v19
	v_lshl_add_u64 v[4:5], v[4:5], 1, s[86:87]
	v_lshl_add_u64 v[4:5], s[34:35], 1, v[4:5]
	v_lshl_add_u64 v[4:5], v[4:5], 0, v[2:3]
	global_store_dwordx4 v[4:5], v[14:17], off sc1
	ds_read2_b32 v[4:5], v135 offset0:8 offset1:41
	ds_read2_b32 v[18:19], v135 offset0:74 offset1:107
	ds_read2_b32 v[14:15], v135 offset0:140 offset1:173
	ds_read2_b32 v[16:17], v135 offset0:206 offset1:239
	v_add_u32_e32 v21, s14, v132
	s_cmp_gt_i32 s25, 1
	s_mov_b64 s[0:1], -1
	s_cbranch_scc0 .LBB0_1641
	s_movk_i32 s0, 0xaff
	v_cmp_lt_i32_e32 vcc, s0, v21
	v_lshlrev_b32_e32 v23, 1, v21
	v_and_b32_e32 v22, 0x7f, v21
	s_and_saveexec_b64 s[0:1], vcc
	s_xor_b64 s[0:1], exec, s[0:1]
	v_add_u32_e32 v20, 0x7fffea00, v23
	v_and_b32_e32 v20, 0x7fffff00, v20
	s_movk_i32 s4, 0x80
	v_or3_b32 v20, v22, v20, s4
	s_andn2_saveexec_b64 s[0:1], s[0:1]
	s_movk_i32 s4, 0xff00
	v_and_or_b32 v20, v23, s4, v22
	s_or_b64 exec, exec, s[0:1]
	s_mov_b64 s[0:1], 0

; #define GAS __attribute__((address_space(1)))
; #define LAS __attribute__((address_space(3)))
; __device__ __forceinline__ unsigned pk2(float lo, float hi) { return f2bf(lo) | (f2bf(hi) << 16); }
; __device__ __forceinline__ int wrow_map(int mode, int n) {
;     if (mode == 1) { if (n >= 1024 && n < 2048) { const int d = n & 63; return (n & ~63) + 32 * ((d >> 4) & 1) + 8 * ((d >> 2) & 3) + 4 * (d >> 5) + (d & 3); } return n; }
;     if (mode == 2) { if (n < DFF) return 256 * (n >> 7) + (n & 127); const int n2 = n - DFF; return 256 * (n2 >> 7) + 128 + (n2 & 127); }
;     return n;
; template <bool WT> __device__ __forceinline__ void cvt_process(const CvtItem& ci, const CvtLoad& L, LAS float* scr, int lane) {
;     ...
;     for (int j = 0; j < 4; ++j) { const int n = (lane >> 3) + 8 * j; const LAS float* s = scr + (8 * c) * 33 + n;
;         v4u o; o.x = pk2(s[0 * 33] * g0.x, s[1 * 33] * g0.y); o.y = pk2(s[2 * 33] * g0.z, s[3 * 33] * g0.w); o.z = pk2(s[4 * 33] * g1.x, s[5 * 33] * g1.y); o.w = pk2(s[6 * 33] * g1.z, s[7 * 33] * g1.w);
;         GAS v4u* dp = (GAS v4u*)(ci.WT + (size_t)(ci.row_off + wrow_map(ci.mode, n0 + n)) * ci.K + k0 + 8 * c);
;         if constexpr (WT) asm volatile("global_store_dwordx4 %0, %1, off sc1" :: "v"(dp), "v"(o) : "memory"); else if (ci.late) __builtin_nontemporal_store(o, dp); else *dp = o; }
.LBB0_1645:
	s_waitcnt lgkmcnt(2)
	v_mov_b32_e32 v23, v18
	v_mov_b32_e32 v18, v5
	v_mov_b32_e32 v22, v4
	v_pk_mul_f32 v[4:5], v[10:11], v[18:19]
	s_waitcnt lgkmcnt(0)
	v_mov_b32_e32 v19, v16
	v_mov_b32_e32 v16, v15
	v_mov_b32_e32 v18, v14
	v_pk_mul_f32 v[14:15], v[6:7], v[16:17]
	v_pk_mul_f32 v[22:23], v[12:13], v[22:23]
	v_pk_mul_f32 v[18:19], v[8:9], v[18:19]
	v_cvt_pk_bf16_f32 v16, v18, v14
	v_cvt_pk_bf16_f32 v14, v22, v4
	v_add_u32_e32 v4, s16, v20
	v_cvt_pk_bf16_f32 v17, v19, v15
	v_cvt_pk_bf16_f32 v15, v23, v5
	v_ashrrev_i32_e32 v5, 31, v4
	v_mul_lo_u32 v18, s84, v5
	v_mul_lo_u32 v19, s85, v4
	v_mad_u64_u32 v[4:5], s[0:1], s84, v4, 0
	v_add3_u32 v5, v5, v18, v19
	v_lshl_add_u64 v[4:5], v[4:5], 1, s[86:87]
	v_lshl_add_u64 v[4:5], s[34:35], 1, v[4:5]
	v_lshl_add_u64 v[4:5], v[4:5], 0, v[2:3]
	global_store_dwordx4 v[4:5], v[14:17], off sc1
	ds_read2_b32 v[4:5], v135 offset0:16 offset1:49
	ds_read2_b32 v[18:19], v135 offset0:82 offset1:115
	ds_read2_b32 v[14:15], v135 offset0:148 offset1:181
	ds_read2_b32 v[16:17], v135 offset0:214 offset1:247
	v_add_u32_e32 v21, s14, v133
	s_cmp_gt_i32 s25, 1
	s_mov_b64 s[0:1], -1
	s_cbranch_scc0 .LBB0_1651
	s_movk_i32 s0, 0xaff
	v_cmp_lt_i32_e32 vcc, s0, v21
	v_lshlrev_b32_e32 v23, 1, v21
	v_and_b32_e32 v22, 0x7f, v21
	s_and_saveexec_b64 s[0:1], vcc
	s_xor_b64 s[0:1], exec, s[0:1]
	v_add_u32_e32 v20, 0x7fffea00, v23
	v_and_b32_e32 v20, 0x7fffff00, v20
	s_movk_i32 s4, 0x80
	v_or3_b32 v20, v22, v20, s4
	s_andn2_saveexec_b64 s[0:1], s[0:1]
	s_movk_i32 s4, 0xff00
	v_and_or_b32 v20, v23, s4, v22
	s_or_b64 exec, exec, s[0:1]
	s_mov_b64 s[0:1], 0

; #define GAS __attribute__((address_space(1)))
; #define LAS __attribute__((address_space(3)))
; __device__ __forceinline__ unsigned pk2(float lo, float hi) { return f2bf(lo) | (f2bf(hi) << 16); }
; __device__ __forceinline__ int wrow_map(int mode, int n) {
;     if (mode == 1) { if (n >= 1024 && n < 2048) { const int d = n & 63; return (n & ~63) + 32 * ((d >> 4) & 1) + 8 * ((d >> 2) & 3) + 4 * (d >> 5) + (d & 3); } return n; }
;     if (mode == 2) { if (n < DFF) return 256 * (n >> 7) + (n & 127); const int n2 = n - DFF; return 256 * (n2 >> 7) + 128 + (n2 & 127); }
;     return n;
; template <bool WT> __device__ __forceinline__ void cvt_process(const CvtItem& ci, const CvtLoad& L, LAS float* scr, int lane) {
;     ...
;     for (int j = 0; j < 4; ++j) { const int n = (lane >> 3) + 8 * j; const LAS float* s = scr + (8 * c) * 33 + n;
;         v4u o; o.x = pk2(s[0 * 33] * g0.x, s[1 * 33] * g0.y); o.y = pk2(s[2 * 33] * g0.z, s[3 * 33] * g0.w); o.z = pk2(s[4 * 33] * g1.x, s[5 * 33] * g1.y); o.w = pk2(s[6 * 33] * g1.z, s[7 * 33] * g1.w);
;         GAS v4u* dp = (GAS v4u*)(ci.WT + (size_t)(ci.row_off + wrow_map(ci.mode, n0 + n)) * ci.K + k0 + 8 * c);
;         if constexpr (WT) asm volatile("global_store_dwordx4 %0, %1, off sc1" :: "v"(dp), "v"(o) : "memory"); else if (ci.late) __builtin_nontemporal_store(o, dp); else *dp = o; }
.LBB0_1655:
	s_waitcnt lgkmcnt(2)
	v_mov_b32_e32 v23, v18
	v_mov_b32_e32 v18, v5
	v_mov_b32_e32 v22, v4
	v_pk_mul_f32 v[4:5], v[10:11], v[18:19]
	s_waitcnt lgkmcnt(0)
	v_mov_b32_e32 v19, v16
	v_mov_b32_e32 v16, v15
	v_mov_b32_e32 v18, v14
	v_pk_mul_f32 v[14:15], v[6:7], v[16:17]
	v_pk_mul_f32 v[22:23], v[12:13], v[22:23]
	v_pk_mul_f32 v[18:19], v[8:9], v[18:19]
	v_cvt_pk_bf16_f32 v16, v18, v14
	v_cvt_pk_bf16_f32 v14, v22, v4
	v_add_u32_e32 v4, s16, v20
	v_cvt_pk_bf16_f32 v17, v19, v15
	v_cvt_pk_bf16_f32 v15, v23, v5
	v_ashrrev_i32_e32 v5, 31, v4
	v_mul_lo_u32 v18, s84, v5
	v_mul_lo_u32 v19, s85, v4
	v_mad_u64_u32 v[4:5], s[0:1], s84, v4, 0
	v_add3_u32 v5, v5, v18, v19
	v_lshl_add_u64 v[4:5], v[4:5], 1, s[86:87]
	v_lshl_add_u64 v[4:5], s[34:35], 1, v[4:5]
	v_lshl_add_u64 v[4:5], v[4:5], 0, v[2:3]
	global_store_dwordx4 v[4:5], v[14:17], off sc1
	ds_read2_b32 v[14:15], v135 offset0:24 offset1:57
	ds_read2_b32 v[16:17], v135 offset0:90 offset1:123
	ds_read2_b32 v[4:5], v135 offset0:156 offset1:189
	ds_read2_b32 v[18:19], v135 offset0:222 offset1:255
	v_add_u32_e32 v21, s14, v134
	s_cmp_gt_i32 s25, 1
	s_mov_b64 s[0:1], -1
	s_cbranch_scc0 .LBB0_1661
	s_movk_i32 s0, 0xaff
	v_cmp_lt_i32_e32 vcc, s0, v21
	v_lshlrev_b32_e32 v23, 1, v21
	v_and_b32_e32 v22, 0x7f, v21
	s_and_saveexec_b64 s[0:1], vcc
	s_xor_b64 s[0:1], exec, s[0:1]
	v_add_u32_e32 v20, 0x7fffea00, v23
	v_and_b32_e32 v20, 0x7fffff00, v20
	s_movk_i32 s4, 0x80
	v_or3_b32 v20, v22, v20, s4
	s_andn2_saveexec_b64 s[0:1], s[0:1]
	s_movk_i32 s4, 0xff00
	v_and_or_b32 v20, v23, s4, v22
	s_or_b64 exec, exec, s[0:1]
	s_mov_b64 s[0:1], 0
